# static priority: every per-cluster s_setprio flip deleted, one s_setprio 1 for waves 4-7 at entry
# baseline (speedup 1.0000x reference)
_Z8mega_fwd8MegaArgs:
	v_readfirstlane_b32 s33, v0
	s_nop 3
	s_and_b32 s33, s33, 0x3ff
	s_lshr_b32 s33, s33, 6
	s_cmp_ge_u32 s33, 4
	s_cbranch_scc0 .Lprio_done
	s_setprio 1
.Lprio_done:
	s_load_dword s20, s[0:1], 0xb0
	s_load_dwordx4 s[16:19], s[0:1], 0xa0
	s_load_dwordx8 s[4:11], s[0:1], 0x80
	s_mov_b32 s66, s2
	s_add_u32 s2, s0, 0xb0
	s_addc_u32 s3, s1, 0
	s_mov_b32 s96, s66
	s_waitcnt lgkmcnt(0)
	v_writelane_b32 v251, s4, 0
	s_nop 1
	v_writelane_b32 v251, s5, 1
	v_writelane_b32 v251, s6, 2
	v_writelane_b32 v251, s7, 3
	v_writelane_b32 v251, s8, 4
	v_writelane_b32 v251, s9, 5
	v_writelane_b32 v251, s10, 6
	v_writelane_b32 v251, s11, 7
	v_writelane_b32 v251, s2, 8
	s_nop 1
	v_writelane_b32 v251, s3, 9
	s_and_b32 s2, s20, 7
	s_cmp_lg_u32 s2, 0
	s_cbranch_scc1 .LBB0_2
	s_ashr_i32 s3, s66, 31
	s_lshr_b32 s3, s3, 29
	s_add_i32 s3, s66, s3
	s_and_b32 s4, s3, -8
	s_ashr_i32 s2, s20, 3
	s_sub_i32 s4, s66, s4
	s_mul_i32 s2, s2, s4
	s_ashr_i32 s3, s3, 3
	s_add_i32 s96, s2, s3

.LBB0_121:
	s_add_u32 s38, s12, 0x80
	s_addc_u32 s39, s13, 0
	s_waitcnt vmcnt(8)
	s_and_b64 s[14:15], s[14:15], exec
	s_waitcnt lgkmcnt(0)
	s_cselect_b32 s14, s57, s58
	s_cselect_b32 s41, s31, s39
	s_cselect_b32 s40, s30, s38
	s_cselect_b32 s15, s7, s59
	s_add_u32 s38, s14, 0x8000
	s_addc_u32 s39, s15, 0
	s_barrier
	s_waitcnt lgkmcnt(0)
	v_mfma_f32_16x16x32_bf16 v[64:67], v[104:107], v[128:131], v[64:67]
	v_mfma_f32_16x16x32_bf16 v[60:63], v[112:115], v[128:131], v[60:63]
	v_mfma_f32_16x16x32_bf16 v[56:59], v[104:107], v[120:123], v[56:59]
	v_mfma_f32_16x16x32_bf16 v[52:55], v[112:115], v[120:123], v[52:55]
	v_mfma_f32_16x16x32_bf16 v[40:43], v[104:107], v[96:99], v[40:43]
	v_mfma_f32_16x16x32_bf16 v[36:39], v[112:115], v[96:99], v[36:39]
	v_mfma_f32_16x16x32_bf16 v[24:27], v[104:107], v[88:91], v[24:27]
	v_mfma_f32_16x16x32_bf16 v[20:23], v[112:115], v[88:91], v[20:23]
	v_mfma_f32_16x16x32_bf16 v[64:67], v[108:111], v[132:135], v[64:67]
	v_mfma_f32_16x16x32_bf16 v[60:63], v[116:119], v[132:135], v[60:63]
	v_mfma_f32_16x16x32_bf16 v[56:59], v[108:111], v[124:127], v[56:59]
	v_mfma_f32_16x16x32_bf16 v[52:55], v[116:119], v[124:127], v[52:55]
	v_mfma_f32_16x16x32_bf16 v[40:43], v[108:111], v[100:103], v[40:43]
	v_mfma_f32_16x16x32_bf16 v[36:39], v[116:119], v[100:103], v[36:39]
	v_mfma_f32_16x16x32_bf16 v[24:27], v[108:111], v[92:95], v[24:27]
	v_mfma_f32_16x16x32_bf16 v[20:23], v[116:119], v[92:95], v[20:23]
	v_mfma_f32_16x16x32_bf16 v[48:51], v[68:71], v[128:131], v[48:51]
	v_mfma_f32_16x16x32_bf16 v[44:47], v[76:79], v[128:131], v[44:47]
	v_mfma_f32_16x16x32_bf16 v[32:35], v[68:71], v[120:123], v[32:35]
	v_mfma_f32_16x16x32_bf16 v[28:31], v[76:79], v[120:123], v[28:31]
	v_mfma_f32_16x16x32_bf16 v[16:19], v[68:71], v[96:99], v[16:19]
	v_mfma_f32_16x16x32_bf16 v[12:15], v[76:79], v[96:99], v[12:15]
	v_mfma_f32_16x16x32_bf16 v[8:11], v[68:71], v[88:91], v[8:11]
	v_mfma_f32_16x16x32_bf16 v[4:7], v[76:79], v[88:91], v[4:7]
	v_mfma_f32_16x16x32_bf16 v[48:51], v[72:75], v[132:135], v[48:51]
	v_mfma_f32_16x16x32_bf16 v[44:47], v[80:83], v[132:135], v[44:47]
	v_mfma_f32_16x16x32_bf16 v[32:35], v[72:75], v[124:127], v[32:35]
	v_mfma_f32_16x16x32_bf16 v[28:31], v[80:83], v[124:127], v[28:31]
	v_mfma_f32_16x16x32_bf16 v[16:19], v[72:75], v[100:103], v[16:19]
	v_mfma_f32_16x16x32_bf16 v[12:15], v[80:83], v[100:103], v[12:15]
	v_mfma_f32_16x16x32_bf16 v[8:11], v[72:75], v[92:95], v[8:11]
	v_mfma_f32_16x16x32_bf16 v[4:7], v[80:83], v[92:95], v[4:7]
	s_barrier
	s_mov_b32 m0, s43
	v_lshl_add_u64 v[68:69], s[14:15], 0, v[138:139]
	s_add_u32 s62, s14, 0x4000
	global_load_lds_dwordx4 v[68:69], off
	v_lshl_add_u64 v[68:69], s[14:15], 0, v[136:137]
	s_mov_b32 m0, s44
	s_addc_u32 s63, s15, 0
	global_load_lds_dwordx4 v[68:69], off
	v_lshl_add_u64 v[68:69], s[62:63], 0, v[138:139]
	s_mov_b32 m0, s45
	v_mov_b32_e32 v143, v3
	global_load_lds_dwordx4 v[68:69], off
	v_lshl_add_u64 v[68:69], s[62:63], 0, v[136:137]
	s_mov_b32 m0, s47
	v_lshl_add_u64 v[166:167], s[40:41], 0, v[2:3]
	global_load_lds_dwordx4 v[68:69], off
	s_mov_b32 m0, s42
	v_lshl_add_u64 v[168:169], s[40:41], 0, v[142:143]
	global_load_lds_dwordx4 v2, s[40:41]
	s_mov_b32 m0, s48
	s_nop 0
	global_load_lds_dwordx4 v142, s[40:41]
	s_waitcnt vmcnt(8)
	s_waitcnt lgkmcnt(0)
	s_barrier
	s_barrier
	s_add_i32 s61, 0, 0x18000
	s_add_i32 s62, 0, 0x1c000
	v_add_u32_e32 v80, s61, v160
	v_add_u32_e32 v100, s62, v160
	ds_read_b128 v[68:71], v80
	ds_read_b128 v[72:75], v80 offset:1024
	ds_read_b128 v[76:79], v80 offset:2048
	ds_read_b128 v[80:83], v80 offset:3072
	ds_read_b128 v[88:91], v100
	ds_read_b128 v[92:95], v100 offset:1024
	ds_read_b128 v[96:99], v100 offset:2048
	ds_read_b128 v[100:103], v100 offset:3072
	s_mov_b32 m0, s49
	v_lshl_add_u64 v[154:155], s[40:41], 0, v[154:155]
	ds_read_b128 v[104:107], v163 offset:32768
	ds_read_b128 v[108:111], v163 offset:33792
	ds_read_b128 v[112:115], v163 offset:34816
	ds_read_b128 v[116:119], v163 offset:35840
	ds_read_b128 v[120:123], v163 offset:36864
	ds_read_b128 v[124:127], v163 offset:37888
	ds_read_b128 v[128:131], v163 offset:38912
	ds_read_b128 v[132:135], v163 offset:39936
	global_load_lds_dwordx4 v[154:155], off
	v_lshl_add_u64 v[152:153], s[40:41], 0, v[152:153]
	s_mov_b32 m0, s50
	s_nop 0
	global_load_lds_dwordx4 v[152:153], off
	s_waitcnt vmcnt(8)
	s_waitcnt lgkmcnt(0)
	s_barrier
	s_waitcnt lgkmcnt(0)
	v_mfma_f32_16x16x32_bf16 v[64:67], v[68:71], v[104:107], v[64:67]
	v_mfma_f32_16x16x32_bf16 v[60:63], v[76:79], v[104:107], v[60:63]
	v_mfma_f32_16x16x32_bf16 v[56:59], v[68:71], v[112:115], v[56:59]
	v_mfma_f32_16x16x32_bf16 v[52:55], v[76:79], v[112:115], v[52:55]
	v_mfma_f32_16x16x32_bf16 v[40:43], v[68:71], v[120:123], v[40:43]
	v_mfma_f32_16x16x32_bf16 v[36:39], v[76:79], v[120:123], v[36:39]
	v_mfma_f32_16x16x32_bf16 v[24:27], v[68:71], v[128:131], v[24:27]
	v_mfma_f32_16x16x32_bf16 v[20:23], v[76:79], v[128:131], v[20:23]
	v_mfma_f32_16x16x32_bf16 v[64:67], v[72:75], v[108:111], v[64:67]
	v_mfma_f32_16x16x32_bf16 v[60:63], v[80:83], v[108:111], v[60:63]
	v_mfma_f32_16x16x32_bf16 v[56:59], v[72:75], v[116:119], v[56:59]
	v_mfma_f32_16x16x32_bf16 v[52:55], v[80:83], v[116:119], v[52:55]
	v_mfma_f32_16x16x32_bf16 v[40:43], v[72:75], v[124:127], v[40:43]
	v_mfma_f32_16x16x32_bf16 v[36:39], v[80:83], v[124:127], v[36:39]
	v_mfma_f32_16x16x32_bf16 v[24:27], v[72:75], v[132:135], v[24:27]
	v_mfma_f32_16x16x32_bf16 v[20:23], v[80:83], v[132:135], v[20:23]
	v_mfma_f32_16x16x32_bf16 v[48:51], v[88:91], v[104:107], v[48:51]
	v_mfma_f32_16x16x32_bf16 v[44:47], v[96:99], v[104:107], v[44:47]
	v_mfma_f32_16x16x32_bf16 v[32:35], v[88:91], v[112:115], v[32:35]
	v_mfma_f32_16x16x32_bf16 v[28:31], v[96:99], v[112:115], v[28:31]
	v_mfma_f32_16x16x32_bf16 v[16:19], v[88:91], v[120:123], v[16:19]
	v_mfma_f32_16x16x32_bf16 v[12:15], v[96:99], v[120:123], v[12:15]
	v_mfma_f32_16x16x32_bf16 v[8:11], v[88:91], v[128:131], v[8:11]
	v_mfma_f32_16x16x32_bf16 v[4:7], v[96:99], v[128:131], v[4:7]
	v_mfma_f32_16x16x32_bf16 v[48:51], v[92:95], v[108:111], v[48:51]
	v_mfma_f32_16x16x32_bf16 v[44:47], v[100:103], v[108:111], v[44:47]
	v_mfma_f32_16x16x32_bf16 v[32:35], v[92:95], v[116:119], v[32:35]
	v_mfma_f32_16x16x32_bf16 v[28:31], v[100:103], v[116:119], v[28:31]
	v_mfma_f32_16x16x32_bf16 v[16:19], v[92:95], v[124:127], v[16:19]
	v_mfma_f32_16x16x32_bf16 v[12:15], v[100:103], v[124:127], v[12:15]
	v_mfma_f32_16x16x32_bf16 v[8:11], v[92:95], v[132:135], v[8:11]
	v_mfma_f32_16x16x32_bf16 v[4:7], v[100:103], v[132:135], v[4:7]
	s_barrier
	s_add_i32 s40, s61, s33
	v_lshl_add_u64 v[68:69], s[38:39], 0, v[138:139]
	s_mov_b32 m0, s40
	s_nop 0
	global_load_lds_dwordx4 v[68:69], off
	s_add_i32 m0, s40, 0x2000
	s_add_u32 s14, s14, 0xc000
	v_lshl_add_u64 v[68:69], s[38:39], 0, v[136:137]
	s_addc_u32 s15, s15, 0
	s_add_i32 s38, s62, s33
	global_load_lds_dwordx4 v[68:69], off
	v_lshl_add_u64 v[68:69], s[14:15], 0, v[138:139]
	s_mov_b32 m0, s38
	s_nop 0
	global_load_lds_dwordx4 v[68:69], off
	v_lshl_add_u64 v[68:69], s[14:15], 0, v[136:137]
	s_add_i32 m0, s38, 0x2000
	s_nop 0
	global_load_lds_dwordx4 v[68:69], off
	v_lshl_add_u64 v[68:69], v[166:167], 0, s[36:37]
	s_mov_b32 m0, s51
	s_nop 0
	global_load_lds_dwordx4 v[68:69], off
	v_lshl_add_u64 v[68:69], v[168:169], 0, s[36:37]
	s_mov_b32 m0, s52
	s_nop 0
	global_load_lds_dwordx4 v[68:69], off
	s_waitcnt vmcnt(8)
	s_waitcnt lgkmcnt(0)
	s_barrier
	s_barrier
	s_add_i32 s60, s60, 2
	s_add_u32 s58, s58, 0x10000
	s_addc_u32 s59, s59, 0
	s_add_u32 s12, s12, 0x100
	s_addc_u32 s13, s13, 0
	s_cmp_gt_u32 s60, 29
	s_cbranch_scc1 .LBB0_124

.LBB0_144:
	s_add_u32 s40, s14, 0x80
	s_addc_u32 s41, s15, 0
	s_waitcnt vmcnt(8)
	s_and_b64 s[38:39], s[38:39], exec
	s_waitcnt lgkmcnt(0)
	s_cselect_b32 s38, s13, s60
	s_cselect_b32 s43, s31, s41
	s_cselect_b32 s42, s30, s40
	s_cselect_b32 s39, s9, s61
	s_add_u32 s40, s38, 0x8000
	s_addc_u32 s41, s39, 0
	s_barrier
	s_waitcnt lgkmcnt(0)
	v_mfma_f32_16x16x32_bf16 v[132:135], v[152:155], v[192:195], v[132:135]
	v_mfma_f32_16x16x32_bf16 v[128:131], v[160:163], v[192:195], v[128:131]
	v_mfma_f32_16x16x32_bf16 v[124:127], v[152:155], v[184:187], v[124:127]
	v_mfma_f32_16x16x32_bf16 v[116:119], v[160:163], v[184:187], v[116:119]
	v_mfma_f32_16x16x32_bf16 v[108:111], v[152:155], v[176:179], v[108:111]
	v_mfma_f32_16x16x32_bf16 v[100:103], v[160:163], v[176:179], v[100:103]
	v_mfma_f32_16x16x32_bf16 v[92:95], v[152:155], v[168:171], v[92:95]
	v_mfma_f32_16x16x32_bf16 v[80:83], v[160:163], v[168:171], v[80:83]
	v_mfma_f32_16x16x32_bf16 v[132:135], v[156:159], v[196:199], v[132:135]
	v_mfma_f32_16x16x32_bf16 v[128:131], v[164:167], v[196:199], v[128:131]
	v_mfma_f32_16x16x32_bf16 v[124:127], v[156:159], v[188:191], v[124:127]
	v_mfma_f32_16x16x32_bf16 v[116:119], v[164:167], v[188:191], v[116:119]
	v_mfma_f32_16x16x32_bf16 v[108:111], v[156:159], v[180:183], v[108:111]
	v_mfma_f32_16x16x32_bf16 v[100:103], v[164:167], v[180:183], v[100:103]
	v_mfma_f32_16x16x32_bf16 v[92:95], v[156:159], v[172:175], v[92:95]
	v_mfma_f32_16x16x32_bf16 v[80:83], v[164:167], v[172:175], v[80:83]
	v_mfma_f32_16x16x32_bf16 v[120:123], v[136:139], v[192:195], v[120:123]
	v_mfma_f32_16x16x32_bf16 v[112:115], v[144:147], v[192:195], v[112:115]
	v_mfma_f32_16x16x32_bf16 v[104:107], v[136:139], v[184:187], v[104:107]
	v_mfma_f32_16x16x32_bf16 v[96:99], v[144:147], v[184:187], v[96:99]
	v_mfma_f32_16x16x32_bf16 v[88:91], v[136:139], v[176:179], v[88:91]
	v_mfma_f32_16x16x32_bf16 v[76:79], v[144:147], v[176:179], v[76:79]
	v_mfma_f32_16x16x32_bf16 v[72:75], v[136:139], v[168:171], v[72:75]
	v_mfma_f32_16x16x32_bf16 v[68:71], v[144:147], v[168:171], v[68:71]
	v_mfma_f32_16x16x32_bf16 v[120:123], v[140:143], v[196:199], v[120:123]
	v_mfma_f32_16x16x32_bf16 v[112:115], v[148:151], v[196:199], v[112:115]
	v_mfma_f32_16x16x32_bf16 v[104:107], v[140:143], v[188:191], v[104:107]
	v_mfma_f32_16x16x32_bf16 v[96:99], v[148:151], v[188:191], v[96:99]
	v_mfma_f32_16x16x32_bf16 v[88:91], v[140:143], v[180:183], v[88:91]
	v_mfma_f32_16x16x32_bf16 v[76:79], v[148:151], v[180:183], v[76:79]
	v_mfma_f32_16x16x32_bf16 v[72:75], v[140:143], v[172:175], v[72:75]
	v_mfma_f32_16x16x32_bf16 v[68:71], v[148:151], v[172:175], v[68:71]
	s_barrier
	s_mov_b32 m0, s48
	v_lshl_add_u64 v[204:205], s[38:39], 0, v[210:211]
	s_add_u32 s64, s38, 0x4000
	ds_read_b128 v[168:171], v244 offset:16384
	ds_read_b128 v[172:175], v244 offset:17408
	ds_read_b128 v[176:179], v244 offset:18432
	ds_read_b128 v[180:183], v244 offset:19456
	ds_read_b128 v[184:187], v244 offset:20480
	ds_read_b128 v[188:191], v244 offset:21504
	ds_read_b128 v[192:195], v244 offset:22528
	ds_read_b128 v[196:199], v244 offset:23552
	global_load_lds_dwordx4 v[204:205], off
	v_lshl_add_u64 v[204:205], s[38:39], 0, v[208:209]
	s_mov_b32 m0, s49
	s_addc_u32 s65, s39, 0
	global_load_lds_dwordx4 v[204:205], off
	v_lshl_add_u64 v[204:205], s[64:65], 0, v[210:211]
	s_mov_b32 m0, s50
	v_mov_b32_e32 v215, v3
	global_load_lds_dwordx4 v[204:205], off
	v_lshl_add_u64 v[204:205], s[64:65], 0, v[208:209]
	s_mov_b32 m0, s51
	v_lshl_add_u64 v[248:249], s[42:43], 0, v[214:215]
	global_load_lds_dwordx4 v[204:205], off
	s_mov_b32 m0, s47
	v_lshl_add_u64 v[204:205], s[42:43], 0, v[2:3]
	global_load_lds_dwordx4 v2, s[42:43]
	s_mov_b32 m0, s52
	s_nop 0
	global_load_lds_dwordx4 v214, s[42:43]
	s_waitcnt vmcnt(8)
	s_waitcnt lgkmcnt(0)
	s_barrier
	s_waitcnt lgkmcnt(0)
	v_mfma_f32_16x16x32_bf16 v[64:67], v[152:155], v[168:171], v[64:67]
	v_mfma_f32_16x16x32_bf16 v[60:63], v[160:163], v[168:171], v[60:63]
	v_mfma_f32_16x16x32_bf16 v[56:59], v[152:155], v[176:179], v[56:59]
	v_mfma_f32_16x16x32_bf16 v[48:51], v[160:163], v[176:179], v[48:51]
	v_mfma_f32_16x16x32_bf16 v[40:43], v[152:155], v[184:187], v[40:43]
	v_mfma_f32_16x16x32_bf16 v[32:35], v[160:163], v[184:187], v[32:35]
	v_mfma_f32_16x16x32_bf16 v[24:27], v[152:155], v[192:195], v[24:27]
	v_mfma_f32_16x16x32_bf16 v[16:19], v[160:163], v[192:195], v[16:19]
	v_mfma_f32_16x16x32_bf16 v[64:67], v[156:159], v[172:175], v[64:67]
	v_mfma_f32_16x16x32_bf16 v[60:63], v[164:167], v[172:175], v[60:63]
	v_mfma_f32_16x16x32_bf16 v[56:59], v[156:159], v[180:183], v[56:59]
	v_mfma_f32_16x16x32_bf16 v[48:51], v[164:167], v[180:183], v[48:51]
	v_mfma_f32_16x16x32_bf16 v[40:43], v[156:159], v[188:191], v[40:43]
	v_mfma_f32_16x16x32_bf16 v[32:35], v[164:167], v[188:191], v[32:35]
	v_mfma_f32_16x16x32_bf16 v[24:27], v[156:159], v[196:199], v[24:27]
	v_mfma_f32_16x16x32_bf16 v[16:19], v[164:167], v[196:199], v[16:19]
	v_mfma_f32_16x16x32_bf16 v[52:55], v[136:139], v[168:171], v[52:55]
	v_mfma_f32_16x16x32_bf16 v[44:47], v[144:147], v[168:171], v[44:47]
	v_mfma_f32_16x16x32_bf16 v[36:39], v[136:139], v[176:179], v[36:39]
	v_mfma_f32_16x16x32_bf16 v[28:31], v[144:147], v[176:179], v[28:31]
	v_mfma_f32_16x16x32_bf16 v[20:23], v[136:139], v[184:187], v[20:23]
	v_mfma_f32_16x16x32_bf16 v[12:15], v[144:147], v[184:187], v[12:15]
	v_mfma_f32_16x16x32_bf16 v[8:11], v[136:139], v[192:195], v[8:11]
	v_mfma_f32_16x16x32_bf16 v[4:7], v[144:147], v[192:195], v[4:7]
	v_mfma_f32_16x16x32_bf16 v[52:55], v[140:143], v[172:175], v[52:55]
	v_mfma_f32_16x16x32_bf16 v[44:47], v[148:151], v[172:175], v[44:47]
	v_mfma_f32_16x16x32_bf16 v[36:39], v[140:143], v[180:183], v[36:39]
	v_mfma_f32_16x16x32_bf16 v[28:31], v[148:151], v[180:183], v[28:31]
	v_mfma_f32_16x16x32_bf16 v[20:23], v[140:143], v[188:191], v[20:23]
	v_mfma_f32_16x16x32_bf16 v[12:15], v[148:151], v[188:191], v[12:15]
	v_mfma_f32_16x16x32_bf16 v[8:11], v[140:143], v[196:199], v[8:11]
	v_mfma_f32_16x16x32_bf16 v[4:7], v[148:151], v[196:199], v[4:7]
	s_barrier
	s_add_i32 s63, 0, 0x18000
	s_add_i32 s64, 0, 0x1c000
	v_add_u32_e32 v148, s63, v243
	v_add_u32_e32 v164, s64, v243
	ds_read_b128 v[136:139], v148
	ds_read_b128 v[140:143], v148 offset:1024
	ds_read_b128 v[144:147], v148 offset:2048
	ds_read_b128 v[148:151], v148 offset:3072
	ds_read_b128 v[152:155], v164
	ds_read_b128 v[156:159], v164 offset:1024
	ds_read_b128 v[160:163], v164 offset:2048
	ds_read_b128 v[164:167], v164 offset:3072
	s_mov_b32 m0, s53
	v_lshl_add_u64 v[226:227], s[42:43], 0, v[226:227]
	ds_read_b128 v[168:171], v244 offset:32768
	ds_read_b128 v[172:175], v244 offset:33792
	ds_read_b128 v[176:179], v244 offset:34816
	ds_read_b128 v[180:183], v244 offset:35840
	ds_read_b128 v[184:187], v244 offset:36864
	ds_read_b128 v[188:191], v244 offset:37888
	ds_read_b128 v[192:195], v244 offset:38912
	ds_read_b128 v[196:199], v244 offset:39936
	global_load_lds_dwordx4 v[226:227], off
	v_lshl_add_u64 v[224:225], s[42:43], 0, v[224:225]
	s_mov_b32 m0, s54
	s_nop 0
	global_load_lds_dwordx4 v[224:225], off
	s_waitcnt vmcnt(8)
	s_waitcnt lgkmcnt(0)
	s_barrier
	s_waitcnt lgkmcnt(0)
	v_mfma_f32_16x16x32_bf16 v[132:135], v[136:139], v[168:171], v[132:135]
	v_mfma_f32_16x16x32_bf16 v[128:131], v[144:147], v[168:171], v[128:131]
	v_mfma_f32_16x16x32_bf16 v[124:127], v[136:139], v[176:179], v[124:127]
	v_mfma_f32_16x16x32_bf16 v[116:119], v[144:147], v[176:179], v[116:119]
	v_mfma_f32_16x16x32_bf16 v[108:111], v[136:139], v[184:187], v[108:111]
	v_mfma_f32_16x16x32_bf16 v[100:103], v[144:147], v[184:187], v[100:103]
	v_mfma_f32_16x16x32_bf16 v[92:95], v[136:139], v[192:195], v[92:95]
	v_mfma_f32_16x16x32_bf16 v[80:83], v[144:147], v[192:195], v[80:83]
	v_mfma_f32_16x16x32_bf16 v[132:135], v[140:143], v[172:175], v[132:135]
	v_mfma_f32_16x16x32_bf16 v[128:131], v[148:151], v[172:175], v[128:131]
	v_mfma_f32_16x16x32_bf16 v[124:127], v[140:143], v[180:183], v[124:127]
	v_mfma_f32_16x16x32_bf16 v[116:119], v[148:151], v[180:183], v[116:119]
	v_mfma_f32_16x16x32_bf16 v[108:111], v[140:143], v[188:191], v[108:111]
	v_mfma_f32_16x16x32_bf16 v[100:103], v[148:151], v[188:191], v[100:103]
	v_mfma_f32_16x16x32_bf16 v[92:95], v[140:143], v[196:199], v[92:95]
	v_mfma_f32_16x16x32_bf16 v[80:83], v[148:151], v[196:199], v[80:83]
	v_mfma_f32_16x16x32_bf16 v[120:123], v[152:155], v[168:171], v[120:123]
	v_mfma_f32_16x16x32_bf16 v[112:115], v[160:163], v[168:171], v[112:115]
	v_mfma_f32_16x16x32_bf16 v[104:107], v[152:155], v[176:179], v[104:107]
	v_mfma_f32_16x16x32_bf16 v[96:99], v[160:163], v[176:179], v[96:99]
	v_mfma_f32_16x16x32_bf16 v[88:91], v[152:155], v[184:187], v[88:91]
	v_mfma_f32_16x16x32_bf16 v[76:79], v[160:163], v[184:187], v[76:79]
	v_mfma_f32_16x16x32_bf16 v[72:75], v[152:155], v[192:195], v[72:75]
	v_mfma_f32_16x16x32_bf16 v[68:71], v[160:163], v[192:195], v[68:71]
	v_mfma_f32_16x16x32_bf16 v[120:123], v[156:159], v[172:175], v[120:123]
	v_mfma_f32_16x16x32_bf16 v[112:115], v[164:167], v[172:175], v[112:115]
	v_mfma_f32_16x16x32_bf16 v[104:107], v[156:159], v[180:183], v[104:107]
	v_mfma_f32_16x16x32_bf16 v[96:99], v[164:167], v[180:183], v[96:99]
	v_mfma_f32_16x16x32_bf16 v[88:91], v[156:159], v[188:191], v[88:91]
	v_mfma_f32_16x16x32_bf16 v[76:79], v[164:167], v[188:191], v[76:79]
	v_mfma_f32_16x16x32_bf16 v[72:75], v[156:159], v[196:199], v[72:75]
	v_mfma_f32_16x16x32_bf16 v[68:71], v[164:167], v[196:199], v[68:71]
	s_barrier
	s_add_i32 s42, s63, s45
	v_lshl_add_u64 v[224:225], s[40:41], 0, v[210:211]
	s_mov_b32 m0, s42
	ds_read_b128 v[168:171], v244 offset:49152
	ds_read_b128 v[172:175], v244 offset:50176
	ds_read_b128 v[176:179], v244 offset:51200
	ds_read_b128 v[180:183], v244 offset:52224
	ds_read_b128 v[184:187], v244 offset:53248
	ds_read_b128 v[188:191], v244 offset:54272
	ds_read_b128 v[192:195], v244 offset:55296
	ds_read_b128 v[196:199], v244 offset:56320
	global_load_lds_dwordx4 v[224:225], off
	s_add_i32 m0, s42, 0x2000
	s_add_u32 s38, s38, 0xc000
	v_lshl_add_u64 v[224:225], s[40:41], 0, v[208:209]
	s_addc_u32 s39, s39, 0
	s_add_i32 s40, s64, s45
	global_load_lds_dwordx4 v[224:225], off
	v_lshl_add_u64 v[224:225], s[38:39], 0, v[210:211]
	s_mov_b32 m0, s40
	v_lshl_add_u64 v[204:205], v[204:205], 0, s[36:37]
	global_load_lds_dwordx4 v[224:225], off
	v_lshl_add_u64 v[224:225], s[38:39], 0, v[208:209]
	s_add_i32 m0, s40, 0x2000
	s_nop 0
	global_load_lds_dwordx4 v[224:225], off
	s_mov_b32 m0, s55
	s_nop 0
	global_load_lds_dwordx4 v[204:205], off
	v_lshl_add_u64 v[204:205], v[248:249], 0, s[36:37]
	s_mov_b32 m0, s56
	s_nop 0
	global_load_lds_dwordx4 v[204:205], off
	s_waitcnt vmcnt(8)
	s_waitcnt lgkmcnt(0)
	s_barrier
	s_waitcnt lgkmcnt(0)
	v_mfma_f32_16x16x32_bf16 v[64:67], v[136:139], v[168:171], v[64:67]
	v_mfma_f32_16x16x32_bf16 v[60:63], v[144:147], v[168:171], v[60:63]
	v_mfma_f32_16x16x32_bf16 v[56:59], v[136:139], v[176:179], v[56:59]
	v_mfma_f32_16x16x32_bf16 v[48:51], v[144:147], v[176:179], v[48:51]
	v_mfma_f32_16x16x32_bf16 v[40:43], v[136:139], v[184:187], v[40:43]
	v_mfma_f32_16x16x32_bf16 v[32:35], v[144:147], v[184:187], v[32:35]
	v_mfma_f32_16x16x32_bf16 v[24:27], v[136:139], v[192:195], v[24:27]
	v_mfma_f32_16x16x32_bf16 v[16:19], v[144:147], v[192:195], v[16:19]
	v_mfma_f32_16x16x32_bf16 v[64:67], v[140:143], v[172:175], v[64:67]
	v_mfma_f32_16x16x32_bf16 v[60:63], v[148:151], v[172:175], v[60:63]
	v_mfma_f32_16x16x32_bf16 v[56:59], v[140:143], v[180:183], v[56:59]
	v_mfma_f32_16x16x32_bf16 v[48:51], v[148:151], v[180:183], v[48:51]
	v_mfma_f32_16x16x32_bf16 v[40:43], v[140:143], v[188:191], v[40:43]
	v_mfma_f32_16x16x32_bf16 v[32:35], v[148:151], v[188:191], v[32:35]
	v_mfma_f32_16x16x32_bf16 v[24:27], v[140:143], v[196:199], v[24:27]
	v_mfma_f32_16x16x32_bf16 v[16:19], v[148:151], v[196:199], v[16:19]
	v_mfma_f32_16x16x32_bf16 v[52:55], v[152:155], v[168:171], v[52:55]
	v_mfma_f32_16x16x32_bf16 v[44:47], v[160:163], v[168:171], v[44:47]
	v_mfma_f32_16x16x32_bf16 v[36:39], v[152:155], v[176:179], v[36:39]
	v_mfma_f32_16x16x32_bf16 v[28:31], v[160:163], v[176:179], v[28:31]
	v_mfma_f32_16x16x32_bf16 v[20:23], v[152:155], v[184:187], v[20:23]
	v_mfma_f32_16x16x32_bf16 v[12:15], v[160:163], v[184:187], v[12:15]
	v_mfma_f32_16x16x32_bf16 v[8:11], v[152:155], v[192:195], v[8:11]
	v_mfma_f32_16x16x32_bf16 v[4:7], v[160:163], v[192:195], v[4:7]
	v_mfma_f32_16x16x32_bf16 v[52:55], v[156:159], v[172:175], v[52:55]
	v_mfma_f32_16x16x32_bf16 v[44:47], v[164:167], v[172:175], v[44:47]
	v_mfma_f32_16x16x32_bf16 v[36:39], v[156:159], v[180:183], v[36:39]
	v_mfma_f32_16x16x32_bf16 v[28:31], v[164:167], v[180:183], v[28:31]
	v_mfma_f32_16x16x32_bf16 v[20:23], v[156:159], v[188:191], v[20:23]
	v_mfma_f32_16x16x32_bf16 v[12:15], v[164:167], v[188:191], v[12:15]
	v_mfma_f32_16x16x32_bf16 v[8:11], v[156:159], v[196:199], v[8:11]
	v_mfma_f32_16x16x32_bf16 v[4:7], v[164:167], v[196:199], v[4:7]
	s_barrier
	s_add_i32 s62, s62, 2
	s_add_u32 s60, s60, 0x10000
	s_addc_u32 s61, s61, 0
	s_add_u32 s14, s14, 0x100
	s_addc_u32 s15, s15, 0
	s_cmp_gt_u32 s62, 29
	s_cbranch_scc1 .LBB0_147

.LBB0_294:
	s_add_u32 s40, s14, 0x80
	s_addc_u32 s41, s15, 0
	s_waitcnt vmcnt(8)
	s_and_b64 s[38:39], s[38:39], exec
	s_waitcnt lgkmcnt(0)
	s_cselect_b32 s38, s13, s59
	s_cselect_b32 s43, s1, s41
	s_cselect_b32 s42, s0, s40
	s_cselect_b32 s39, s9, s60
	s_add_u32 s40, s38, 0x8000
	s_addc_u32 s41, s39, 0
	s_barrier
	s_waitcnt lgkmcnt(0)
	v_mfma_f32_16x16x32_bf16 v[132:135], v[152:155], v[192:195], v[132:135]
	v_mfma_f32_16x16x32_bf16 v[128:131], v[160:163], v[192:195], v[128:131]
	v_mfma_f32_16x16x32_bf16 v[124:127], v[152:155], v[184:187], v[124:127]
	v_mfma_f32_16x16x32_bf16 v[120:123], v[160:163], v[184:187], v[120:123]
	v_mfma_f32_16x16x32_bf16 v[108:111], v[152:155], v[176:179], v[108:111]
	v_mfma_f32_16x16x32_bf16 v[104:107], v[160:163], v[176:179], v[104:107]
	v_mfma_f32_16x16x32_bf16 v[92:95], v[152:155], v[168:171], v[92:95]
	v_mfma_f32_16x16x32_bf16 v[88:91], v[160:163], v[168:171], v[88:91]
	v_mfma_f32_16x16x32_bf16 v[132:135], v[156:159], v[196:199], v[132:135]
	v_mfma_f32_16x16x32_bf16 v[128:131], v[164:167], v[196:199], v[128:131]
	v_mfma_f32_16x16x32_bf16 v[124:127], v[156:159], v[188:191], v[124:127]
	v_mfma_f32_16x16x32_bf16 v[120:123], v[164:167], v[188:191], v[120:123]
	v_mfma_f32_16x16x32_bf16 v[108:111], v[156:159], v[180:183], v[108:111]
	v_mfma_f32_16x16x32_bf16 v[104:107], v[164:167], v[180:183], v[104:107]
	v_mfma_f32_16x16x32_bf16 v[92:95], v[156:159], v[172:175], v[92:95]
	v_mfma_f32_16x16x32_bf16 v[88:91], v[164:167], v[172:175], v[88:91]
	v_mfma_f32_16x16x32_bf16 v[116:119], v[136:139], v[192:195], v[116:119]
	v_mfma_f32_16x16x32_bf16 v[112:115], v[144:147], v[192:195], v[112:115]
	v_mfma_f32_16x16x32_bf16 v[100:103], v[136:139], v[184:187], v[100:103]
	v_mfma_f32_16x16x32_bf16 v[96:99], v[144:147], v[184:187], v[96:99]
	v_mfma_f32_16x16x32_bf16 v[80:83], v[136:139], v[176:179], v[80:83]
	v_mfma_f32_16x16x32_bf16 v[76:79], v[144:147], v[176:179], v[76:79]
	v_mfma_f32_16x16x32_bf16 v[72:75], v[136:139], v[168:171], v[72:75]
	v_mfma_f32_16x16x32_bf16 v[68:71], v[144:147], v[168:171], v[68:71]
	v_mfma_f32_16x16x32_bf16 v[116:119], v[140:143], v[196:199], v[116:119]
	v_mfma_f32_16x16x32_bf16 v[112:115], v[148:151], v[196:199], v[112:115]
	v_mfma_f32_16x16x32_bf16 v[100:103], v[140:143], v[188:191], v[100:103]
	v_mfma_f32_16x16x32_bf16 v[96:99], v[148:151], v[188:191], v[96:99]
	v_mfma_f32_16x16x32_bf16 v[80:83], v[140:143], v[180:183], v[80:83]
	v_mfma_f32_16x16x32_bf16 v[76:79], v[148:151], v[180:183], v[76:79]
	v_mfma_f32_16x16x32_bf16 v[72:75], v[140:143], v[172:175], v[72:75]
	v_mfma_f32_16x16x32_bf16 v[68:71], v[148:151], v[172:175], v[68:71]
	s_barrier
	s_mov_b32 m0, s47
	v_lshl_add_u64 v[204:205], s[38:39], 0, v[210:211]
	s_add_u32 s62, s38, 0x4000
	ds_read_b128 v[168:171], v244 offset:16384
	ds_read_b128 v[172:175], v244 offset:17408
	ds_read_b128 v[176:179], v244 offset:18432
	ds_read_b128 v[180:183], v244 offset:19456
	ds_read_b128 v[184:187], v244 offset:20480
	ds_read_b128 v[188:191], v244 offset:21504
	ds_read_b128 v[192:195], v244 offset:22528
	ds_read_b128 v[196:199], v244 offset:23552
	global_load_lds_dwordx4 v[204:205], off
	v_lshl_add_u64 v[204:205], s[38:39], 0, v[208:209]
	s_mov_b32 m0, s48
	s_addc_u32 s63, s39, 0
	global_load_lds_dwordx4 v[204:205], off
	v_lshl_add_u64 v[204:205], s[62:63], 0, v[210:211]
	s_mov_b32 m0, s49
	v_mov_b32_e32 v215, v3
	global_load_lds_dwordx4 v[204:205], off
	v_lshl_add_u64 v[204:205], s[62:63], 0, v[208:209]
	s_mov_b32 m0, s50
	v_lshl_add_u64 v[248:249], s[42:43], 0, v[214:215]
	global_load_lds_dwordx4 v[204:205], off
	s_mov_b32 m0, s45
	v_lshl_add_u64 v[204:205], s[42:43], 0, v[2:3]
	global_load_lds_dwordx4 v2, s[42:43]
	s_mov_b32 m0, s51
	s_nop 0
	global_load_lds_dwordx4 v214, s[42:43]
	s_waitcnt vmcnt(8)
	s_waitcnt lgkmcnt(0)
	s_barrier
	s_waitcnt lgkmcnt(0)
	v_mfma_f32_16x16x32_bf16 v[64:67], v[152:155], v[168:171], v[64:67]
	v_mfma_f32_16x16x32_bf16 v[60:63], v[160:163], v[168:171], v[60:63]
	v_mfma_f32_16x16x32_bf16 v[56:59], v[152:155], v[176:179], v[56:59]
	v_mfma_f32_16x16x32_bf16 v[52:55], v[160:163], v[176:179], v[52:55]
	v_mfma_f32_16x16x32_bf16 v[40:43], v[152:155], v[184:187], v[40:43]
	v_mfma_f32_16x16x32_bf16 v[36:39], v[160:163], v[184:187], v[36:39]
	v_mfma_f32_16x16x32_bf16 v[24:27], v[152:155], v[192:195], v[24:27]
	v_mfma_f32_16x16x32_bf16 v[20:23], v[160:163], v[192:195], v[20:23]
	v_mfma_f32_16x16x32_bf16 v[64:67], v[156:159], v[172:175], v[64:67]
	v_mfma_f32_16x16x32_bf16 v[60:63], v[164:167], v[172:175], v[60:63]
	v_mfma_f32_16x16x32_bf16 v[56:59], v[156:159], v[180:183], v[56:59]
	v_mfma_f32_16x16x32_bf16 v[52:55], v[164:167], v[180:183], v[52:55]
	v_mfma_f32_16x16x32_bf16 v[40:43], v[156:159], v[188:191], v[40:43]
	v_mfma_f32_16x16x32_bf16 v[36:39], v[164:167], v[188:191], v[36:39]
	v_mfma_f32_16x16x32_bf16 v[24:27], v[156:159], v[196:199], v[24:27]
	v_mfma_f32_16x16x32_bf16 v[20:23], v[164:167], v[196:199], v[20:23]
	v_mfma_f32_16x16x32_bf16 v[48:51], v[136:139], v[168:171], v[48:51]
	v_mfma_f32_16x16x32_bf16 v[44:47], v[144:147], v[168:171], v[44:47]
	v_mfma_f32_16x16x32_bf16 v[32:35], v[136:139], v[176:179], v[32:35]
	v_mfma_f32_16x16x32_bf16 v[28:31], v[144:147], v[176:179], v[28:31]
	v_mfma_f32_16x16x32_bf16 v[16:19], v[136:139], v[184:187], v[16:19]
	v_mfma_f32_16x16x32_bf16 v[12:15], v[144:147], v[184:187], v[12:15]
	v_mfma_f32_16x16x32_bf16 v[8:11], v[136:139], v[192:195], v[8:11]
	v_mfma_f32_16x16x32_bf16 v[4:7], v[144:147], v[192:195], v[4:7]
	v_mfma_f32_16x16x32_bf16 v[48:51], v[140:143], v[172:175], v[48:51]
	v_mfma_f32_16x16x32_bf16 v[44:47], v[148:151], v[172:175], v[44:47]
	v_mfma_f32_16x16x32_bf16 v[32:35], v[140:143], v[180:183], v[32:35]
	v_mfma_f32_16x16x32_bf16 v[28:31], v[148:151], v[180:183], v[28:31]
	v_mfma_f32_16x16x32_bf16 v[16:19], v[140:143], v[188:191], v[16:19]
	v_mfma_f32_16x16x32_bf16 v[12:15], v[148:151], v[188:191], v[12:15]
	v_mfma_f32_16x16x32_bf16 v[8:11], v[140:143], v[196:199], v[8:11]
	v_mfma_f32_16x16x32_bf16 v[4:7], v[148:151], v[196:199], v[4:7]
	s_barrier
	s_add_i32 s62, 0, 0x18000
	s_add_i32 s63, 0, 0x1c000
	v_add_u32_e32 v148, s62, v243
	v_add_u32_e32 v164, s63, v243
	ds_read_b128 v[136:139], v148
	ds_read_b128 v[140:143], v148 offset:1024
	ds_read_b128 v[144:147], v148 offset:2048
	ds_read_b128 v[148:151], v148 offset:3072
	ds_read_b128 v[152:155], v164
	ds_read_b128 v[156:159], v164 offset:1024
	ds_read_b128 v[160:163], v164 offset:2048
	ds_read_b128 v[164:167], v164 offset:3072
	s_mov_b32 m0, s52
	v_lshl_add_u64 v[226:227], s[42:43], 0, v[226:227]
	ds_read_b128 v[168:171], v244 offset:32768
	ds_read_b128 v[172:175], v244 offset:33792
	ds_read_b128 v[176:179], v244 offset:34816
	ds_read_b128 v[180:183], v244 offset:35840
	ds_read_b128 v[184:187], v244 offset:36864
	ds_read_b128 v[188:191], v244 offset:37888
	ds_read_b128 v[192:195], v244 offset:38912
	ds_read_b128 v[196:199], v244 offset:39936
	global_load_lds_dwordx4 v[226:227], off
	v_lshl_add_u64 v[224:225], s[42:43], 0, v[224:225]
	s_mov_b32 m0, s53
	s_nop 0
	global_load_lds_dwordx4 v[224:225], off
	s_waitcnt vmcnt(8)
	s_waitcnt lgkmcnt(0)
	s_barrier
	s_waitcnt lgkmcnt(0)
	v_mfma_f32_16x16x32_bf16 v[132:135], v[136:139], v[168:171], v[132:135]
	v_mfma_f32_16x16x32_bf16 v[128:131], v[144:147], v[168:171], v[128:131]
	v_mfma_f32_16x16x32_bf16 v[124:127], v[136:139], v[176:179], v[124:127]
	v_mfma_f32_16x16x32_bf16 v[120:123], v[144:147], v[176:179], v[120:123]
	v_mfma_f32_16x16x32_bf16 v[108:111], v[136:139], v[184:187], v[108:111]
	v_mfma_f32_16x16x32_bf16 v[104:107], v[144:147], v[184:187], v[104:107]
	v_mfma_f32_16x16x32_bf16 v[92:95], v[136:139], v[192:195], v[92:95]
	v_mfma_f32_16x16x32_bf16 v[88:91], v[144:147], v[192:195], v[88:91]
	v_mfma_f32_16x16x32_bf16 v[132:135], v[140:143], v[172:175], v[132:135]
	v_mfma_f32_16x16x32_bf16 v[128:131], v[148:151], v[172:175], v[128:131]
	v_mfma_f32_16x16x32_bf16 v[124:127], v[140:143], v[180:183], v[124:127]
	v_mfma_f32_16x16x32_bf16 v[120:123], v[148:151], v[180:183], v[120:123]
	v_mfma_f32_16x16x32_bf16 v[108:111], v[140:143], v[188:191], v[108:111]
	v_mfma_f32_16x16x32_bf16 v[104:107], v[148:151], v[188:191], v[104:107]
	v_mfma_f32_16x16x32_bf16 v[92:95], v[140:143], v[196:199], v[92:95]
	v_mfma_f32_16x16x32_bf16 v[88:91], v[148:151], v[196:199], v[88:91]
	v_mfma_f32_16x16x32_bf16 v[116:119], v[152:155], v[168:171], v[116:119]
	v_mfma_f32_16x16x32_bf16 v[112:115], v[160:163], v[168:171], v[112:115]
	v_mfma_f32_16x16x32_bf16 v[100:103], v[152:155], v[176:179], v[100:103]
	v_mfma_f32_16x16x32_bf16 v[96:99], v[160:163], v[176:179], v[96:99]
	v_mfma_f32_16x16x32_bf16 v[80:83], v[152:155], v[184:187], v[80:83]
	v_mfma_f32_16x16x32_bf16 v[76:79], v[160:163], v[184:187], v[76:79]
	v_mfma_f32_16x16x32_bf16 v[72:75], v[152:155], v[192:195], v[72:75]
	v_mfma_f32_16x16x32_bf16 v[68:71], v[160:163], v[192:195], v[68:71]
	v_mfma_f32_16x16x32_bf16 v[116:119], v[156:159], v[172:175], v[116:119]
	v_mfma_f32_16x16x32_bf16 v[112:115], v[164:167], v[172:175], v[112:115]
	v_mfma_f32_16x16x32_bf16 v[100:103], v[156:159], v[180:183], v[100:103]
	v_mfma_f32_16x16x32_bf16 v[96:99], v[164:167], v[180:183], v[96:99]
	v_mfma_f32_16x16x32_bf16 v[80:83], v[156:159], v[188:191], v[80:83]
	v_mfma_f32_16x16x32_bf16 v[76:79], v[164:167], v[188:191], v[76:79]
	v_mfma_f32_16x16x32_bf16 v[72:75], v[156:159], v[196:199], v[72:75]
	v_mfma_f32_16x16x32_bf16 v[68:71], v[164:167], v[196:199], v[68:71]
	s_barrier
	s_add_i32 s42, s62, s44
	v_lshl_add_u64 v[224:225], s[40:41], 0, v[210:211]
	s_mov_b32 m0, s42
	ds_read_b128 v[168:171], v244 offset:49152
	ds_read_b128 v[172:175], v244 offset:50176
	ds_read_b128 v[176:179], v244 offset:51200
	ds_read_b128 v[180:183], v244 offset:52224
	ds_read_b128 v[184:187], v244 offset:53248
	ds_read_b128 v[188:191], v244 offset:54272
	ds_read_b128 v[192:195], v244 offset:55296
	ds_read_b128 v[196:199], v244 offset:56320
	global_load_lds_dwordx4 v[224:225], off
	s_add_i32 m0, s42, 0x2000
	s_add_u32 s38, s38, 0xc000
	v_lshl_add_u64 v[224:225], s[40:41], 0, v[208:209]
	s_addc_u32 s39, s39, 0
	s_add_i32 s40, s63, s44
	global_load_lds_dwordx4 v[224:225], off
	v_lshl_add_u64 v[224:225], s[38:39], 0, v[210:211]
	s_mov_b32 m0, s40
	v_lshl_add_u64 v[204:205], v[204:205], 0, s[36:37]
	global_load_lds_dwordx4 v[224:225], off
	v_lshl_add_u64 v[224:225], s[38:39], 0, v[208:209]
	s_add_i32 m0, s40, 0x2000
	s_nop 0
	global_load_lds_dwordx4 v[224:225], off
	s_mov_b32 m0, s54
	s_nop 0
	global_load_lds_dwordx4 v[204:205], off
	v_lshl_add_u64 v[204:205], v[248:249], 0, s[36:37]
	s_mov_b32 m0, s55
	s_nop 0
	global_load_lds_dwordx4 v[204:205], off
	s_waitcnt vmcnt(8)
	s_waitcnt lgkmcnt(0)
	s_barrier
	s_waitcnt lgkmcnt(0)
	v_mfma_f32_16x16x32_bf16 v[64:67], v[136:139], v[168:171], v[64:67]
	v_mfma_f32_16x16x32_bf16 v[60:63], v[144:147], v[168:171], v[60:63]
	v_mfma_f32_16x16x32_bf16 v[56:59], v[136:139], v[176:179], v[56:59]
	v_mfma_f32_16x16x32_bf16 v[52:55], v[144:147], v[176:179], v[52:55]
	v_mfma_f32_16x16x32_bf16 v[40:43], v[136:139], v[184:187], v[40:43]
	v_mfma_f32_16x16x32_bf16 v[36:39], v[144:147], v[184:187], v[36:39]
	v_mfma_f32_16x16x32_bf16 v[24:27], v[136:139], v[192:195], v[24:27]
	v_mfma_f32_16x16x32_bf16 v[20:23], v[144:147], v[192:195], v[20:23]
	v_mfma_f32_16x16x32_bf16 v[64:67], v[140:143], v[172:175], v[64:67]
	v_mfma_f32_16x16x32_bf16 v[60:63], v[148:151], v[172:175], v[60:63]
	v_mfma_f32_16x16x32_bf16 v[56:59], v[140:143], v[180:183], v[56:59]
	v_mfma_f32_16x16x32_bf16 v[52:55], v[148:151], v[180:183], v[52:55]
	v_mfma_f32_16x16x32_bf16 v[40:43], v[140:143], v[188:191], v[40:43]
	v_mfma_f32_16x16x32_bf16 v[36:39], v[148:151], v[188:191], v[36:39]
	v_mfma_f32_16x16x32_bf16 v[24:27], v[140:143], v[196:199], v[24:27]
	v_mfma_f32_16x16x32_bf16 v[20:23], v[148:151], v[196:199], v[20:23]
	v_mfma_f32_16x16x32_bf16 v[48:51], v[152:155], v[168:171], v[48:51]
	v_mfma_f32_16x16x32_bf16 v[44:47], v[160:163], v[168:171], v[44:47]
	v_mfma_f32_16x16x32_bf16 v[32:35], v[152:155], v[176:179], v[32:35]
	v_mfma_f32_16x16x32_bf16 v[28:31], v[160:163], v[176:179], v[28:31]
	v_mfma_f32_16x16x32_bf16 v[16:19], v[152:155], v[184:187], v[16:19]
	v_mfma_f32_16x16x32_bf16 v[12:15], v[160:163], v[184:187], v[12:15]
	v_mfma_f32_16x16x32_bf16 v[8:11], v[152:155], v[192:195], v[8:11]
	v_mfma_f32_16x16x32_bf16 v[4:7], v[160:163], v[192:195], v[4:7]
	v_mfma_f32_16x16x32_bf16 v[48:51], v[156:159], v[172:175], v[48:51]
	v_mfma_f32_16x16x32_bf16 v[44:47], v[164:167], v[172:175], v[44:47]
	v_mfma_f32_16x16x32_bf16 v[32:35], v[156:159], v[180:183], v[32:35]
	v_mfma_f32_16x16x32_bf16 v[28:31], v[164:167], v[180:183], v[28:31]
	v_mfma_f32_16x16x32_bf16 v[16:19], v[156:159], v[188:191], v[16:19]
	v_mfma_f32_16x16x32_bf16 v[12:15], v[164:167], v[188:191], v[12:15]
	v_mfma_f32_16x16x32_bf16 v[8:11], v[156:159], v[196:199], v[8:11]
	v_mfma_f32_16x16x32_bf16 v[4:7], v[164:167], v[196:199], v[4:7]
	s_barrier
	s_add_i32 s61, s61, 2
	s_add_u32 s59, s59, 0x10000
	s_addc_u32 s60, s60, 0
	s_add_u32 s14, s14, 0x100
	s_addc_u32 s15, s15, 0
	s_cmp_gt_u32 s61, 29
	s_cbranch_scc1 .LBB0_297

.LBB0_498:
	s_add_u32 s38, s12, 0x80
	s_addc_u32 s39, s13, 0
	s_waitcnt vmcnt(8)
	s_and_b64 s[14:15], s[14:15], exec
	s_waitcnt lgkmcnt(0)
	s_cselect_b32 s14, s60, s61
	s_cselect_b32 s41, s31, s39
	s_cselect_b32 s40, s30, s38
	s_cselect_b32 s15, s9, s62
	s_add_u32 s38, s14, 0x8000
	s_addc_u32 s39, s15, 0
	s_barrier
	s_waitcnt lgkmcnt(0)
	v_mfma_f32_16x16x32_bf16 v[132:135], v[152:155], v[192:195], v[132:135]
	v_mfma_f32_16x16x32_bf16 v[128:131], v[160:163], v[192:195], v[128:131]
	v_mfma_f32_16x16x32_bf16 v[124:127], v[152:155], v[184:187], v[124:127]
	v_mfma_f32_16x16x32_bf16 v[120:123], v[160:163], v[184:187], v[120:123]
	v_mfma_f32_16x16x32_bf16 v[108:111], v[152:155], v[176:179], v[108:111]
	v_mfma_f32_16x16x32_bf16 v[104:107], v[160:163], v[176:179], v[104:107]
	v_mfma_f32_16x16x32_bf16 v[92:95], v[152:155], v[168:171], v[92:95]
	v_mfma_f32_16x16x32_bf16 v[88:91], v[160:163], v[168:171], v[88:91]
	v_mfma_f32_16x16x32_bf16 v[132:135], v[156:159], v[196:199], v[132:135]
	v_mfma_f32_16x16x32_bf16 v[128:131], v[164:167], v[196:199], v[128:131]
	v_mfma_f32_16x16x32_bf16 v[124:127], v[156:159], v[188:191], v[124:127]
	v_mfma_f32_16x16x32_bf16 v[120:123], v[164:167], v[188:191], v[120:123]
	v_mfma_f32_16x16x32_bf16 v[108:111], v[156:159], v[180:183], v[108:111]
	v_mfma_f32_16x16x32_bf16 v[104:107], v[164:167], v[180:183], v[104:107]
	v_mfma_f32_16x16x32_bf16 v[92:95], v[156:159], v[172:175], v[92:95]
	v_mfma_f32_16x16x32_bf16 v[88:91], v[164:167], v[172:175], v[88:91]
	v_mfma_f32_16x16x32_bf16 v[116:119], v[136:139], v[192:195], v[116:119]
	v_mfma_f32_16x16x32_bf16 v[112:115], v[144:147], v[192:195], v[112:115]
	v_mfma_f32_16x16x32_bf16 v[100:103], v[136:139], v[184:187], v[100:103]
	v_mfma_f32_16x16x32_bf16 v[96:99], v[144:147], v[184:187], v[96:99]
	v_mfma_f32_16x16x32_bf16 v[80:83], v[136:139], v[176:179], v[80:83]
	v_mfma_f32_16x16x32_bf16 v[76:79], v[144:147], v[176:179], v[76:79]
	v_mfma_f32_16x16x32_bf16 v[72:75], v[136:139], v[168:171], v[72:75]
	v_mfma_f32_16x16x32_bf16 v[68:71], v[144:147], v[168:171], v[68:71]
	v_mfma_f32_16x16x32_bf16 v[116:119], v[140:143], v[196:199], v[116:119]
	v_mfma_f32_16x16x32_bf16 v[112:115], v[148:151], v[196:199], v[112:115]
	v_mfma_f32_16x16x32_bf16 v[100:103], v[140:143], v[188:191], v[100:103]
	v_mfma_f32_16x16x32_bf16 v[96:99], v[148:151], v[188:191], v[96:99]
	v_mfma_f32_16x16x32_bf16 v[80:83], v[140:143], v[180:183], v[80:83]
	v_mfma_f32_16x16x32_bf16 v[76:79], v[148:151], v[180:183], v[76:79]
	v_mfma_f32_16x16x32_bf16 v[72:75], v[140:143], v[172:175], v[72:75]
	v_mfma_f32_16x16x32_bf16 v[68:71], v[148:151], v[172:175], v[68:71]
	s_barrier
	s_mov_b32 m0, s44
	v_lshl_add_u64 v[246:247], s[14:15], 0, v[210:211]
	s_add_u32 s64, s14, 0x4000
	ds_read_b128 v[168:171], v243 offset:16384
	ds_read_b128 v[172:175], v243 offset:17408
	ds_read_b128 v[176:179], v243 offset:18432
	ds_read_b128 v[180:183], v243 offset:19456
	ds_read_b128 v[184:187], v243 offset:20480
	ds_read_b128 v[188:191], v243 offset:21504
	ds_read_b128 v[192:195], v243 offset:22528
	ds_read_b128 v[196:199], v243 offset:23552
	global_load_lds_dwordx4 v[246:247], off
	v_lshl_add_u64 v[246:247], s[14:15], 0, v[208:209]
	s_mov_b32 m0, s45
	s_addc_u32 s65, s15, 0
	global_load_lds_dwordx4 v[246:247], off
	v_lshl_add_u64 v[246:247], s[64:65], 0, v[210:211]
	s_mov_b32 m0, s47
	v_mov_b32_e32 v215, v3
	global_load_lds_dwordx4 v[246:247], off
	v_lshl_add_u64 v[246:247], s[64:65], 0, v[208:209]
	s_mov_b32 m0, s48
	v_lshl_add_u64 v[248:249], s[40:41], 0, v[214:215]
	global_load_lds_dwordx4 v[246:247], off
	s_mov_b32 m0, s43
	v_lshl_add_u64 v[246:247], s[40:41], 0, v[2:3]
	global_load_lds_dwordx4 v2, s[40:41]
	s_mov_b32 m0, s49
	s_nop 0
	global_load_lds_dwordx4 v214, s[40:41]
	s_waitcnt vmcnt(8)
	s_waitcnt lgkmcnt(0)
	s_barrier
	s_waitcnt lgkmcnt(0)
	v_mfma_f32_16x16x32_bf16 v[64:67], v[152:155], v[168:171], v[64:67]
	v_mfma_f32_16x16x32_bf16 v[60:63], v[160:163], v[168:171], v[60:63]
	v_mfma_f32_16x16x32_bf16 v[56:59], v[152:155], v[176:179], v[56:59]
	v_mfma_f32_16x16x32_bf16 v[52:55], v[160:163], v[176:179], v[52:55]
	v_mfma_f32_16x16x32_bf16 v[40:43], v[152:155], v[184:187], v[40:43]
	v_mfma_f32_16x16x32_bf16 v[36:39], v[160:163], v[184:187], v[36:39]
	v_mfma_f32_16x16x32_bf16 v[24:27], v[152:155], v[192:195], v[24:27]
	v_mfma_f32_16x16x32_bf16 v[20:23], v[160:163], v[192:195], v[20:23]
	v_mfma_f32_16x16x32_bf16 v[64:67], v[156:159], v[172:175], v[64:67]
	v_mfma_f32_16x16x32_bf16 v[60:63], v[164:167], v[172:175], v[60:63]
	v_mfma_f32_16x16x32_bf16 v[56:59], v[156:159], v[180:183], v[56:59]
	v_mfma_f32_16x16x32_bf16 v[52:55], v[164:167], v[180:183], v[52:55]
	v_mfma_f32_16x16x32_bf16 v[40:43], v[156:159], v[188:191], v[40:43]
	v_mfma_f32_16x16x32_bf16 v[36:39], v[164:167], v[188:191], v[36:39]
	v_mfma_f32_16x16x32_bf16 v[24:27], v[156:159], v[196:199], v[24:27]
	v_mfma_f32_16x16x32_bf16 v[20:23], v[164:167], v[196:199], v[20:23]
	v_mfma_f32_16x16x32_bf16 v[48:51], v[136:139], v[168:171], v[48:51]
	v_mfma_f32_16x16x32_bf16 v[44:47], v[144:147], v[168:171], v[44:47]
	v_mfma_f32_16x16x32_bf16 v[32:35], v[136:139], v[176:179], v[32:35]
	v_mfma_f32_16x16x32_bf16 v[28:31], v[144:147], v[176:179], v[28:31]
	v_mfma_f32_16x16x32_bf16 v[16:19], v[136:139], v[184:187], v[16:19]
	v_mfma_f32_16x16x32_bf16 v[12:15], v[144:147], v[184:187], v[12:15]
	v_mfma_f32_16x16x32_bf16 v[8:11], v[136:139], v[192:195], v[8:11]
	v_mfma_f32_16x16x32_bf16 v[4:7], v[144:147], v[192:195], v[4:7]
	v_mfma_f32_16x16x32_bf16 v[48:51], v[140:143], v[172:175], v[48:51]
	v_mfma_f32_16x16x32_bf16 v[44:47], v[148:151], v[172:175], v[44:47]
	v_mfma_f32_16x16x32_bf16 v[32:35], v[140:143], v[180:183], v[32:35]
	v_mfma_f32_16x16x32_bf16 v[28:31], v[148:151], v[180:183], v[28:31]
	v_mfma_f32_16x16x32_bf16 v[16:19], v[140:143], v[188:191], v[16:19]
	v_mfma_f32_16x16x32_bf16 v[12:15], v[148:151], v[188:191], v[12:15]
	v_mfma_f32_16x16x32_bf16 v[8:11], v[140:143], v[196:199], v[8:11]
	v_mfma_f32_16x16x32_bf16 v[4:7], v[148:151], v[196:199], v[4:7]
	s_barrier
	s_add_i32 s64, 0, 0x18000
	s_add_i32 s65, 0, 0x1c000
	v_add_u32_e32 v148, s64, v241
	v_add_u32_e32 v164, s65, v241
	ds_read_b128 v[136:139], v148
	ds_read_b128 v[140:143], v148 offset:1024
	ds_read_b128 v[144:147], v148 offset:2048
	ds_read_b128 v[148:151], v148 offset:3072
	ds_read_b128 v[152:155], v164
	ds_read_b128 v[156:159], v164 offset:1024
	ds_read_b128 v[160:163], v164 offset:2048
	ds_read_b128 v[164:167], v164 offset:3072
	s_mov_b32 m0, s50
	v_lshl_add_u64 v[224:225], s[40:41], 0, v[224:225]
	ds_read_b128 v[168:171], v243 offset:32768
	ds_read_b128 v[172:175], v243 offset:33792
	ds_read_b128 v[176:179], v243 offset:34816
	ds_read_b128 v[180:183], v243 offset:35840
	ds_read_b128 v[184:187], v243 offset:36864
	ds_read_b128 v[188:191], v243 offset:37888
	ds_read_b128 v[192:195], v243 offset:38912
	ds_read_b128 v[196:199], v243 offset:39936
	global_load_lds_dwordx4 v[224:225], off
	v_lshl_add_u64 v[222:223], s[40:41], 0, v[222:223]
	s_mov_b32 m0, s51
	s_nop 0
	global_load_lds_dwordx4 v[222:223], off
	s_waitcnt vmcnt(8)
	s_waitcnt lgkmcnt(0)
	s_barrier
	s_waitcnt lgkmcnt(0)
	v_mfma_f32_16x16x32_bf16 v[132:135], v[136:139], v[168:171], v[132:135]
	v_mfma_f32_16x16x32_bf16 v[128:131], v[144:147], v[168:171], v[128:131]
	v_mfma_f32_16x16x32_bf16 v[124:127], v[136:139], v[176:179], v[124:127]
	v_mfma_f32_16x16x32_bf16 v[120:123], v[144:147], v[176:179], v[120:123]
	v_mfma_f32_16x16x32_bf16 v[108:111], v[136:139], v[184:187], v[108:111]
	v_mfma_f32_16x16x32_bf16 v[104:107], v[144:147], v[184:187], v[104:107]
	v_mfma_f32_16x16x32_bf16 v[92:95], v[136:139], v[192:195], v[92:95]
	v_mfma_f32_16x16x32_bf16 v[88:91], v[144:147], v[192:195], v[88:91]
	v_mfma_f32_16x16x32_bf16 v[132:135], v[140:143], v[172:175], v[132:135]
	v_mfma_f32_16x16x32_bf16 v[128:131], v[148:151], v[172:175], v[128:131]
	v_mfma_f32_16x16x32_bf16 v[124:127], v[140:143], v[180:183], v[124:127]
	v_mfma_f32_16x16x32_bf16 v[120:123], v[148:151], v[180:183], v[120:123]
	v_mfma_f32_16x16x32_bf16 v[108:111], v[140:143], v[188:191], v[108:111]
	v_mfma_f32_16x16x32_bf16 v[104:107], v[148:151], v[188:191], v[104:107]
	v_mfma_f32_16x16x32_bf16 v[92:95], v[140:143], v[196:199], v[92:95]
	v_mfma_f32_16x16x32_bf16 v[88:91], v[148:151], v[196:199], v[88:91]
	v_mfma_f32_16x16x32_bf16 v[116:119], v[152:155], v[168:171], v[116:119]
	v_mfma_f32_16x16x32_bf16 v[112:115], v[160:163], v[168:171], v[112:115]
	v_mfma_f32_16x16x32_bf16 v[100:103], v[152:155], v[176:179], v[100:103]
	v_mfma_f32_16x16x32_bf16 v[96:99], v[160:163], v[176:179], v[96:99]
	v_mfma_f32_16x16x32_bf16 v[80:83], v[152:155], v[184:187], v[80:83]
	v_mfma_f32_16x16x32_bf16 v[76:79], v[160:163], v[184:187], v[76:79]
	v_mfma_f32_16x16x32_bf16 v[72:75], v[152:155], v[192:195], v[72:75]
	v_mfma_f32_16x16x32_bf16 v[68:71], v[160:163], v[192:195], v[68:71]
	v_mfma_f32_16x16x32_bf16 v[116:119], v[156:159], v[172:175], v[116:119]
	v_mfma_f32_16x16x32_bf16 v[112:115], v[164:167], v[172:175], v[112:115]
	v_mfma_f32_16x16x32_bf16 v[100:103], v[156:159], v[180:183], v[100:103]
	v_mfma_f32_16x16x32_bf16 v[96:99], v[164:167], v[180:183], v[96:99]
	v_mfma_f32_16x16x32_bf16 v[80:83], v[156:159], v[188:191], v[80:83]
	v_mfma_f32_16x16x32_bf16 v[76:79], v[164:167], v[188:191], v[76:79]
	v_mfma_f32_16x16x32_bf16 v[72:75], v[156:159], v[196:199], v[72:75]
	v_mfma_f32_16x16x32_bf16 v[68:71], v[164:167], v[196:199], v[68:71]
	s_barrier
	s_add_i32 s40, s64, s42
	v_lshl_add_u64 v[222:223], s[38:39], 0, v[210:211]
	s_mov_b32 m0, s40
	ds_read_b128 v[168:171], v243 offset:49152
	ds_read_b128 v[172:175], v243 offset:50176
	ds_read_b128 v[176:179], v243 offset:51200
	ds_read_b128 v[180:183], v243 offset:52224
	ds_read_b128 v[184:187], v243 offset:53248
	ds_read_b128 v[188:191], v243 offset:54272
	ds_read_b128 v[192:195], v243 offset:55296
	ds_read_b128 v[196:199], v243 offset:56320
	global_load_lds_dwordx4 v[222:223], off
	s_add_i32 m0, s40, 0x2000
	s_add_u32 s14, s14, 0xc000
	v_lshl_add_u64 v[222:223], s[38:39], 0, v[208:209]
	s_addc_u32 s15, s15, 0
	s_add_i32 s38, s65, s42
	global_load_lds_dwordx4 v[222:223], off
	v_lshl_add_u64 v[222:223], s[14:15], 0, v[210:211]
	s_mov_b32 m0, s38
	s_nop 0
	global_load_lds_dwordx4 v[222:223], off
	v_lshl_add_u64 v[222:223], s[14:15], 0, v[208:209]
	s_add_i32 m0, s38, 0x2000
	s_nop 0
	global_load_lds_dwordx4 v[222:223], off
	v_lshl_add_u64 v[222:223], v[246:247], 0, s[36:37]
	s_mov_b32 m0, s53
	s_nop 0
	global_load_lds_dwordx4 v[222:223], off
	v_lshl_add_u64 v[222:223], v[248:249], 0, s[36:37]
	s_mov_b32 m0, s54
	s_nop 0
	global_load_lds_dwordx4 v[222:223], off
	s_waitcnt vmcnt(8)
	s_waitcnt lgkmcnt(0)
	s_barrier
	s_waitcnt lgkmcnt(0)
	v_mfma_f32_16x16x32_bf16 v[64:67], v[136:139], v[168:171], v[64:67]
	v_mfma_f32_16x16x32_bf16 v[60:63], v[144:147], v[168:171], v[60:63]
	v_mfma_f32_16x16x32_bf16 v[56:59], v[136:139], v[176:179], v[56:59]
	v_mfma_f32_16x16x32_bf16 v[52:55], v[144:147], v[176:179], v[52:55]
	v_mfma_f32_16x16x32_bf16 v[40:43], v[136:139], v[184:187], v[40:43]
	v_mfma_f32_16x16x32_bf16 v[36:39], v[144:147], v[184:187], v[36:39]
	v_mfma_f32_16x16x32_bf16 v[24:27], v[136:139], v[192:195], v[24:27]
	v_mfma_f32_16x16x32_bf16 v[20:23], v[144:147], v[192:195], v[20:23]
	v_mfma_f32_16x16x32_bf16 v[64:67], v[140:143], v[172:175], v[64:67]
	v_mfma_f32_16x16x32_bf16 v[60:63], v[148:151], v[172:175], v[60:63]
	v_mfma_f32_16x16x32_bf16 v[56:59], v[140:143], v[180:183], v[56:59]
	v_mfma_f32_16x16x32_bf16 v[52:55], v[148:151], v[180:183], v[52:55]
	v_mfma_f32_16x16x32_bf16 v[40:43], v[140:143], v[188:191], v[40:43]
	v_mfma_f32_16x16x32_bf16 v[36:39], v[148:151], v[188:191], v[36:39]
	v_mfma_f32_16x16x32_bf16 v[24:27], v[140:143], v[196:199], v[24:27]
	v_mfma_f32_16x16x32_bf16 v[20:23], v[148:151], v[196:199], v[20:23]
	v_mfma_f32_16x16x32_bf16 v[48:51], v[152:155], v[168:171], v[48:51]
	v_mfma_f32_16x16x32_bf16 v[44:47], v[160:163], v[168:171], v[44:47]
	v_mfma_f32_16x16x32_bf16 v[32:35], v[152:155], v[176:179], v[32:35]
	v_mfma_f32_16x16x32_bf16 v[28:31], v[160:163], v[176:179], v[28:31]
	v_mfma_f32_16x16x32_bf16 v[16:19], v[152:155], v[184:187], v[16:19]
	v_mfma_f32_16x16x32_bf16 v[12:15], v[160:163], v[184:187], v[12:15]
	v_mfma_f32_16x16x32_bf16 v[8:11], v[152:155], v[192:195], v[8:11]
	v_mfma_f32_16x16x32_bf16 v[4:7], v[160:163], v[192:195], v[4:7]
	v_mfma_f32_16x16x32_bf16 v[48:51], v[156:159], v[172:175], v[48:51]
	v_mfma_f32_16x16x32_bf16 v[44:47], v[164:167], v[172:175], v[44:47]
	v_mfma_f32_16x16x32_bf16 v[32:35], v[156:159], v[180:183], v[32:35]
	v_mfma_f32_16x16x32_bf16 v[28:31], v[164:167], v[180:183], v[28:31]
	v_mfma_f32_16x16x32_bf16 v[16:19], v[156:159], v[188:191], v[16:19]
	v_mfma_f32_16x16x32_bf16 v[12:15], v[164:167], v[188:191], v[12:15]
	v_mfma_f32_16x16x32_bf16 v[8:11], v[156:159], v[196:199], v[8:11]
	v_mfma_f32_16x16x32_bf16 v[4:7], v[164:167], v[196:199], v[4:7]
	s_barrier
	s_add_i32 s63, s63, 2
	s_add_u32 s61, s61, 0x10000
	s_addc_u32 s62, s62, 0
	s_add_u32 s12, s12, 0x100
	s_addc_u32 s13, s13, 0
	s_cmp_gt_u32 s63, 29
	s_cbranch_scc1 .LBB0_501

.LBB0_835:
	s_add_u32 s40, s14, 0x80
	s_addc_u32 s41, s15, 0
	s_waitcnt vmcnt(8)
	s_and_b64 s[38:39], s[38:39], exec
	s_waitcnt lgkmcnt(0)
	s_cselect_b32 s38, s13, s59
	s_cselect_b32 s43, s1, s41
	s_cselect_b32 s42, s0, s40
	s_cselect_b32 s39, s9, s60
	s_add_u32 s40, s38, 0x8000
	s_addc_u32 s41, s39, 0
	s_barrier
	s_waitcnt lgkmcnt(0)
	v_mfma_f32_16x16x32_bf16 v[132:135], v[152:155], v[192:195], v[132:135]
	v_mfma_f32_16x16x32_bf16 v[128:131], v[160:163], v[192:195], v[128:131]
	v_mfma_f32_16x16x32_bf16 v[124:127], v[152:155], v[184:187], v[124:127]
	v_mfma_f32_16x16x32_bf16 v[120:123], v[160:163], v[184:187], v[120:123]
	v_mfma_f32_16x16x32_bf16 v[108:111], v[152:155], v[176:179], v[108:111]
	v_mfma_f32_16x16x32_bf16 v[104:107], v[160:163], v[176:179], v[104:107]
	v_mfma_f32_16x16x32_bf16 v[92:95], v[152:155], v[168:171], v[92:95]
	v_mfma_f32_16x16x32_bf16 v[88:91], v[160:163], v[168:171], v[88:91]
	v_mfma_f32_16x16x32_bf16 v[132:135], v[156:159], v[196:199], v[132:135]
	v_mfma_f32_16x16x32_bf16 v[128:131], v[164:167], v[196:199], v[128:131]
	v_mfma_f32_16x16x32_bf16 v[124:127], v[156:159], v[188:191], v[124:127]
	v_mfma_f32_16x16x32_bf16 v[120:123], v[164:167], v[188:191], v[120:123]
	v_mfma_f32_16x16x32_bf16 v[108:111], v[156:159], v[180:183], v[108:111]
	v_mfma_f32_16x16x32_bf16 v[104:107], v[164:167], v[180:183], v[104:107]
	v_mfma_f32_16x16x32_bf16 v[92:95], v[156:159], v[172:175], v[92:95]
	v_mfma_f32_16x16x32_bf16 v[88:91], v[164:167], v[172:175], v[88:91]
	v_mfma_f32_16x16x32_bf16 v[116:119], v[136:139], v[192:195], v[116:119]
	v_mfma_f32_16x16x32_bf16 v[112:115], v[144:147], v[192:195], v[112:115]
	v_mfma_f32_16x16x32_bf16 v[100:103], v[136:139], v[184:187], v[100:103]
	v_mfma_f32_16x16x32_bf16 v[96:99], v[144:147], v[184:187], v[96:99]
	v_mfma_f32_16x16x32_bf16 v[80:83], v[136:139], v[176:179], v[80:83]
	v_mfma_f32_16x16x32_bf16 v[76:79], v[144:147], v[176:179], v[76:79]
	v_mfma_f32_16x16x32_bf16 v[72:75], v[136:139], v[168:171], v[72:75]
	v_mfma_f32_16x16x32_bf16 v[68:71], v[144:147], v[168:171], v[68:71]
	v_mfma_f32_16x16x32_bf16 v[116:119], v[140:143], v[196:199], v[116:119]
	v_mfma_f32_16x16x32_bf16 v[112:115], v[148:151], v[196:199], v[112:115]
	v_mfma_f32_16x16x32_bf16 v[100:103], v[140:143], v[188:191], v[100:103]
	v_mfma_f32_16x16x32_bf16 v[96:99], v[148:151], v[188:191], v[96:99]
	v_mfma_f32_16x16x32_bf16 v[80:83], v[140:143], v[180:183], v[80:83]
	v_mfma_f32_16x16x32_bf16 v[76:79], v[148:151], v[180:183], v[76:79]
	v_mfma_f32_16x16x32_bf16 v[72:75], v[140:143], v[172:175], v[72:75]
	v_mfma_f32_16x16x32_bf16 v[68:71], v[148:151], v[172:175], v[68:71]
	s_barrier
	s_mov_b32 m0, s47
	v_lshl_add_u64 v[248:249], s[38:39], 0, v[210:211]
	s_add_u32 s62, s38, 0x4000
	ds_read_b128 v[168:171], v244 offset:16384
	ds_read_b128 v[172:175], v244 offset:17408
	ds_read_b128 v[176:179], v244 offset:18432
	ds_read_b128 v[180:183], v244 offset:19456
	ds_read_b128 v[184:187], v244 offset:20480
	ds_read_b128 v[188:191], v244 offset:21504
	ds_read_b128 v[192:195], v244 offset:22528
	ds_read_b128 v[196:199], v244 offset:23552
	global_load_lds_dwordx4 v[248:249], off
	v_lshl_add_u64 v[248:249], s[38:39], 0, v[208:209]
	s_mov_b32 m0, s48
	s_addc_u32 s63, s39, 0
	global_load_lds_dwordx4 v[248:249], off
	v_lshl_add_u64 v[248:249], s[62:63], 0, v[210:211]
	s_mov_b32 m0, s49
	v_mov_b32_e32 v215, v3
	global_load_lds_dwordx4 v[248:249], off
	v_lshl_add_u64 v[248:249], s[62:63], 0, v[208:209]
	s_mov_b32 m0, s50
	v_lshl_add_u64 v[204:205], s[42:43], 0, v[214:215]
	global_load_lds_dwordx4 v[248:249], off
	s_mov_b32 m0, s45
	v_lshl_add_u64 v[248:249], s[42:43], 0, v[2:3]
	global_load_lds_dwordx4 v2, s[42:43]
	s_mov_b32 m0, s51
	s_nop 0
	global_load_lds_dwordx4 v214, s[42:43]
	s_waitcnt vmcnt(8)
	s_waitcnt lgkmcnt(0)
	s_barrier
	s_waitcnt lgkmcnt(0)
	v_mfma_f32_16x16x32_bf16 v[64:67], v[152:155], v[168:171], v[64:67]
	v_mfma_f32_16x16x32_bf16 v[60:63], v[160:163], v[168:171], v[60:63]
	v_mfma_f32_16x16x32_bf16 v[56:59], v[152:155], v[176:179], v[56:59]
	v_mfma_f32_16x16x32_bf16 v[52:55], v[160:163], v[176:179], v[52:55]
	v_mfma_f32_16x16x32_bf16 v[40:43], v[152:155], v[184:187], v[40:43]
	v_mfma_f32_16x16x32_bf16 v[36:39], v[160:163], v[184:187], v[36:39]
	v_mfma_f32_16x16x32_bf16 v[24:27], v[152:155], v[192:195], v[24:27]
	v_mfma_f32_16x16x32_bf16 v[20:23], v[160:163], v[192:195], v[20:23]
	v_mfma_f32_16x16x32_bf16 v[64:67], v[156:159], v[172:175], v[64:67]
	v_mfma_f32_16x16x32_bf16 v[60:63], v[164:167], v[172:175], v[60:63]
	v_mfma_f32_16x16x32_bf16 v[56:59], v[156:159], v[180:183], v[56:59]
	v_mfma_f32_16x16x32_bf16 v[52:55], v[164:167], v[180:183], v[52:55]
	v_mfma_f32_16x16x32_bf16 v[40:43], v[156:159], v[188:191], v[40:43]
	v_mfma_f32_16x16x32_bf16 v[36:39], v[164:167], v[188:191], v[36:39]
	v_mfma_f32_16x16x32_bf16 v[24:27], v[156:159], v[196:199], v[24:27]
	v_mfma_f32_16x16x32_bf16 v[20:23], v[164:167], v[196:199], v[20:23]
	v_mfma_f32_16x16x32_bf16 v[48:51], v[136:139], v[168:171], v[48:51]
	v_mfma_f32_16x16x32_bf16 v[44:47], v[144:147], v[168:171], v[44:47]
	v_mfma_f32_16x16x32_bf16 v[32:35], v[136:139], v[176:179], v[32:35]
	v_mfma_f32_16x16x32_bf16 v[28:31], v[144:147], v[176:179], v[28:31]
	v_mfma_f32_16x16x32_bf16 v[16:19], v[136:139], v[184:187], v[16:19]
	v_mfma_f32_16x16x32_bf16 v[12:15], v[144:147], v[184:187], v[12:15]
	v_mfma_f32_16x16x32_bf16 v[8:11], v[136:139], v[192:195], v[8:11]
	v_mfma_f32_16x16x32_bf16 v[4:7], v[144:147], v[192:195], v[4:7]
	v_mfma_f32_16x16x32_bf16 v[48:51], v[140:143], v[172:175], v[48:51]
	v_mfma_f32_16x16x32_bf16 v[44:47], v[148:151], v[172:175], v[44:47]
	v_mfma_f32_16x16x32_bf16 v[32:35], v[140:143], v[180:183], v[32:35]
	v_mfma_f32_16x16x32_bf16 v[28:31], v[148:151], v[180:183], v[28:31]
	v_mfma_f32_16x16x32_bf16 v[16:19], v[140:143], v[188:191], v[16:19]
	v_mfma_f32_16x16x32_bf16 v[12:15], v[148:151], v[188:191], v[12:15]
	v_mfma_f32_16x16x32_bf16 v[8:11], v[140:143], v[196:199], v[8:11]
	v_mfma_f32_16x16x32_bf16 v[4:7], v[148:151], v[196:199], v[4:7]
	s_barrier
	s_add_i32 s62, 0, 0x18000
	s_add_i32 s63, 0, 0x1c000
	v_add_u32_e32 v148, s62, v243
	v_add_u32_e32 v164, s63, v243
	ds_read_b128 v[136:139], v148
	ds_read_b128 v[140:143], v148 offset:1024
	ds_read_b128 v[144:147], v148 offset:2048
	ds_read_b128 v[148:151], v148 offset:3072
	ds_read_b128 v[152:155], v164
	ds_read_b128 v[156:159], v164 offset:1024
	ds_read_b128 v[160:163], v164 offset:2048
	ds_read_b128 v[164:167], v164 offset:3072
	s_mov_b32 m0, s52
	v_lshl_add_u64 v[226:227], s[42:43], 0, v[226:227]
	ds_read_b128 v[168:171], v244 offset:32768
	ds_read_b128 v[172:175], v244 offset:33792
	ds_read_b128 v[176:179], v244 offset:34816
	ds_read_b128 v[180:183], v244 offset:35840
	ds_read_b128 v[184:187], v244 offset:36864
	ds_read_b128 v[188:191], v244 offset:37888
	ds_read_b128 v[192:195], v244 offset:38912
	ds_read_b128 v[196:199], v244 offset:39936
	global_load_lds_dwordx4 v[226:227], off
	v_lshl_add_u64 v[224:225], s[42:43], 0, v[224:225]
	s_mov_b32 m0, s53
	s_nop 0
	global_load_lds_dwordx4 v[224:225], off
	s_waitcnt vmcnt(8)
	s_waitcnt lgkmcnt(0)
	s_barrier
	s_waitcnt lgkmcnt(0)
	v_mfma_f32_16x16x32_bf16 v[132:135], v[136:139], v[168:171], v[132:135]
	v_mfma_f32_16x16x32_bf16 v[128:131], v[144:147], v[168:171], v[128:131]
	v_mfma_f32_16x16x32_bf16 v[124:127], v[136:139], v[176:179], v[124:127]
	v_mfma_f32_16x16x32_bf16 v[120:123], v[144:147], v[176:179], v[120:123]
	v_mfma_f32_16x16x32_bf16 v[108:111], v[136:139], v[184:187], v[108:111]
	v_mfma_f32_16x16x32_bf16 v[104:107], v[144:147], v[184:187], v[104:107]
	v_mfma_f32_16x16x32_bf16 v[92:95], v[136:139], v[192:195], v[92:95]
	v_mfma_f32_16x16x32_bf16 v[88:91], v[144:147], v[192:195], v[88:91]
	v_mfma_f32_16x16x32_bf16 v[132:135], v[140:143], v[172:175], v[132:135]
	v_mfma_f32_16x16x32_bf16 v[128:131], v[148:151], v[172:175], v[128:131]
	v_mfma_f32_16x16x32_bf16 v[124:127], v[140:143], v[180:183], v[124:127]
	v_mfma_f32_16x16x32_bf16 v[120:123], v[148:151], v[180:183], v[120:123]
	v_mfma_f32_16x16x32_bf16 v[108:111], v[140:143], v[188:191], v[108:111]
	v_mfma_f32_16x16x32_bf16 v[104:107], v[148:151], v[188:191], v[104:107]
	v_mfma_f32_16x16x32_bf16 v[92:95], v[140:143], v[196:199], v[92:95]
	v_mfma_f32_16x16x32_bf16 v[88:91], v[148:151], v[196:199], v[88:91]
	v_mfma_f32_16x16x32_bf16 v[116:119], v[152:155], v[168:171], v[116:119]
	v_mfma_f32_16x16x32_bf16 v[112:115], v[160:163], v[168:171], v[112:115]
	v_mfma_f32_16x16x32_bf16 v[100:103], v[152:155], v[176:179], v[100:103]
	v_mfma_f32_16x16x32_bf16 v[96:99], v[160:163], v[176:179], v[96:99]
	v_mfma_f32_16x16x32_bf16 v[80:83], v[152:155], v[184:187], v[80:83]
	v_mfma_f32_16x16x32_bf16 v[76:79], v[160:163], v[184:187], v[76:79]
	v_mfma_f32_16x16x32_bf16 v[72:75], v[152:155], v[192:195], v[72:75]
	v_mfma_f32_16x16x32_bf16 v[68:71], v[160:163], v[192:195], v[68:71]
	v_mfma_f32_16x16x32_bf16 v[116:119], v[156:159], v[172:175], v[116:119]
	v_mfma_f32_16x16x32_bf16 v[112:115], v[164:167], v[172:175], v[112:115]
	v_mfma_f32_16x16x32_bf16 v[100:103], v[156:159], v[180:183], v[100:103]
	v_mfma_f32_16x16x32_bf16 v[96:99], v[164:167], v[180:183], v[96:99]
	v_mfma_f32_16x16x32_bf16 v[80:83], v[156:159], v[188:191], v[80:83]
	v_mfma_f32_16x16x32_bf16 v[76:79], v[164:167], v[188:191], v[76:79]
	v_mfma_f32_16x16x32_bf16 v[72:75], v[156:159], v[196:199], v[72:75]
	v_mfma_f32_16x16x32_bf16 v[68:71], v[164:167], v[196:199], v[68:71]
	s_barrier
	s_add_i32 s42, s62, s44
	v_lshl_add_u64 v[224:225], s[40:41], 0, v[210:211]
	s_mov_b32 m0, s42
	ds_read_b128 v[168:171], v244 offset:49152
	ds_read_b128 v[172:175], v244 offset:50176
	ds_read_b128 v[176:179], v244 offset:51200
	ds_read_b128 v[180:183], v244 offset:52224
	ds_read_b128 v[184:187], v244 offset:53248
	ds_read_b128 v[188:191], v244 offset:54272
	ds_read_b128 v[192:195], v244 offset:55296
	ds_read_b128 v[196:199], v244 offset:56320
	global_load_lds_dwordx4 v[224:225], off
	s_add_i32 m0, s42, 0x2000
	s_add_u32 s38, s38, 0xc000
	v_lshl_add_u64 v[224:225], s[40:41], 0, v[208:209]
	s_addc_u32 s39, s39, 0
	s_add_i32 s40, s63, s44
	global_load_lds_dwordx4 v[224:225], off
	v_lshl_add_u64 v[224:225], s[38:39], 0, v[210:211]
	s_mov_b32 m0, s40
	v_lshl_add_u64 v[204:205], v[204:205], 0, s[36:37]
	global_load_lds_dwordx4 v[224:225], off
	v_lshl_add_u64 v[224:225], s[38:39], 0, v[208:209]
	s_add_i32 m0, s40, 0x2000
	s_nop 0
	global_load_lds_dwordx4 v[224:225], off
	v_lshl_add_u64 v[224:225], v[248:249], 0, s[36:37]
	s_mov_b32 m0, s54
	s_nop 0
	global_load_lds_dwordx4 v[224:225], off
	s_mov_b32 m0, s55
	s_nop 0
	global_load_lds_dwordx4 v[204:205], off
	s_waitcnt vmcnt(8)
	s_waitcnt lgkmcnt(0)
	s_barrier
	s_waitcnt lgkmcnt(0)
	v_mfma_f32_16x16x32_bf16 v[64:67], v[136:139], v[168:171], v[64:67]
	v_mfma_f32_16x16x32_bf16 v[60:63], v[144:147], v[168:171], v[60:63]
	v_mfma_f32_16x16x32_bf16 v[56:59], v[136:139], v[176:179], v[56:59]
	v_mfma_f32_16x16x32_bf16 v[52:55], v[144:147], v[176:179], v[52:55]
	v_mfma_f32_16x16x32_bf16 v[40:43], v[136:139], v[184:187], v[40:43]
	v_mfma_f32_16x16x32_bf16 v[36:39], v[144:147], v[184:187], v[36:39]
	v_mfma_f32_16x16x32_bf16 v[24:27], v[136:139], v[192:195], v[24:27]
	v_mfma_f32_16x16x32_bf16 v[20:23], v[144:147], v[192:195], v[20:23]
	v_mfma_f32_16x16x32_bf16 v[64:67], v[140:143], v[172:175], v[64:67]
	v_mfma_f32_16x16x32_bf16 v[60:63], v[148:151], v[172:175], v[60:63]
	v_mfma_f32_16x16x32_bf16 v[56:59], v[140:143], v[180:183], v[56:59]
	v_mfma_f32_16x16x32_bf16 v[52:55], v[148:151], v[180:183], v[52:55]
	v_mfma_f32_16x16x32_bf16 v[40:43], v[140:143], v[188:191], v[40:43]
	v_mfma_f32_16x16x32_bf16 v[36:39], v[148:151], v[188:191], v[36:39]
	v_mfma_f32_16x16x32_bf16 v[24:27], v[140:143], v[196:199], v[24:27]
	v_mfma_f32_16x16x32_bf16 v[20:23], v[148:151], v[196:199], v[20:23]
	v_mfma_f32_16x16x32_bf16 v[48:51], v[152:155], v[168:171], v[48:51]
	v_mfma_f32_16x16x32_bf16 v[44:47], v[160:163], v[168:171], v[44:47]
	v_mfma_f32_16x16x32_bf16 v[32:35], v[152:155], v[176:179], v[32:35]
	v_mfma_f32_16x16x32_bf16 v[28:31], v[160:163], v[176:179], v[28:31]
	v_mfma_f32_16x16x32_bf16 v[16:19], v[152:155], v[184:187], v[16:19]
	v_mfma_f32_16x16x32_bf16 v[12:15], v[160:163], v[184:187], v[12:15]
	v_mfma_f32_16x16x32_bf16 v[8:11], v[152:155], v[192:195], v[8:11]
	v_mfma_f32_16x16x32_bf16 v[4:7], v[160:163], v[192:195], v[4:7]
	v_mfma_f32_16x16x32_bf16 v[48:51], v[156:159], v[172:175], v[48:51]
	v_mfma_f32_16x16x32_bf16 v[44:47], v[164:167], v[172:175], v[44:47]
	v_mfma_f32_16x16x32_bf16 v[32:35], v[156:159], v[180:183], v[32:35]
	v_mfma_f32_16x16x32_bf16 v[28:31], v[164:167], v[180:183], v[28:31]
	v_mfma_f32_16x16x32_bf16 v[16:19], v[156:159], v[188:191], v[16:19]
	v_mfma_f32_16x16x32_bf16 v[12:15], v[164:167], v[188:191], v[12:15]
	v_mfma_f32_16x16x32_bf16 v[8:11], v[156:159], v[196:199], v[8:11]
	v_mfma_f32_16x16x32_bf16 v[4:7], v[164:167], v[196:199], v[4:7]
	s_barrier
	s_add_i32 s61, s61, 2
	s_add_u32 s59, s59, 0x10000
	s_addc_u32 s60, s60, 0
	s_add_u32 s14, s14, 0x100
	s_addc_u32 s15, s15, 0
	s_cmp_gt_u32 s61, 29
	s_cbranch_scc1 .LBB0_838

.LBB0_1175:
	s_waitcnt vmcnt(8)
	s_waitcnt lgkmcnt(0)
	s_barrier
	s_waitcnt lgkmcnt(0)
	v_mfma_f32_16x16x32_bf16 v[132:135], v[152:155], v[180:183], v[132:135]
	v_mfma_f32_16x16x32_bf16 v[128:131], v[160:163], v[180:183], v[128:131]
	v_mfma_f32_16x16x32_bf16 v[124:127], v[152:155], v[176:179], v[124:127]
	v_mfma_f32_16x16x32_bf16 v[120:123], v[160:163], v[176:179], v[120:123]
	v_mfma_f32_16x16x32_bf16 v[116:119], v[152:155], v[172:175], v[116:119]
	v_mfma_f32_16x16x32_bf16 v[112:115], v[160:163], v[172:175], v[112:115]
	v_mfma_f32_16x16x32_bf16 v[108:111], v[152:155], v[168:171], v[108:111]
	v_mfma_f32_16x16x32_bf16 v[104:107], v[160:163], v[168:171], v[104:107]
	v_mfma_f32_16x16x32_bf16 v[132:135], v[156:159], v[196:199], v[132:135]
	v_mfma_f32_16x16x32_bf16 v[128:131], v[164:167], v[196:199], v[128:131]
	v_mfma_f32_16x16x32_bf16 v[124:127], v[156:159], v[192:195], v[124:127]
	v_mfma_f32_16x16x32_bf16 v[120:123], v[164:167], v[192:195], v[120:123]
	v_mfma_f32_16x16x32_bf16 v[116:119], v[156:159], v[188:191], v[116:119]
	v_mfma_f32_16x16x32_bf16 v[112:115], v[164:167], v[188:191], v[112:115]
	v_mfma_f32_16x16x32_bf16 v[108:111], v[156:159], v[184:187], v[108:111]
	v_mfma_f32_16x16x32_bf16 v[104:107], v[164:167], v[184:187], v[104:107]
	v_mfma_f32_16x16x32_bf16 v[100:103], v[136:139], v[180:183], v[100:103]
	v_mfma_f32_16x16x32_bf16 v[96:99], v[144:147], v[180:183], v[96:99]
	v_mfma_f32_16x16x32_bf16 v[92:95], v[136:139], v[176:179], v[92:95]
	v_mfma_f32_16x16x32_bf16 v[88:91], v[144:147], v[176:179], v[88:91]
	v_mfma_f32_16x16x32_bf16 v[80:83], v[136:139], v[172:175], v[80:83]
	v_mfma_f32_16x16x32_bf16 v[76:79], v[144:147], v[172:175], v[76:79]
	v_mfma_f32_16x16x32_bf16 v[72:75], v[136:139], v[168:171], v[72:75]
	v_mfma_f32_16x16x32_bf16 v[68:71], v[144:147], v[168:171], v[68:71]
	v_mfma_f32_16x16x32_bf16 v[100:103], v[140:143], v[196:199], v[100:103]
	v_mfma_f32_16x16x32_bf16 v[96:99], v[148:151], v[196:199], v[96:99]
	v_mfma_f32_16x16x32_bf16 v[92:95], v[140:143], v[192:195], v[92:95]
	v_mfma_f32_16x16x32_bf16 v[88:91], v[148:151], v[192:195], v[88:91]
	v_mfma_f32_16x16x32_bf16 v[80:83], v[140:143], v[188:191], v[80:83]
	v_mfma_f32_16x16x32_bf16 v[76:79], v[148:151], v[188:191], v[76:79]
	v_mfma_f32_16x16x32_bf16 v[72:75], v[140:143], v[184:187], v[72:75]
	v_mfma_f32_16x16x32_bf16 v[68:71], v[148:151], v[184:187], v[68:71]
	s_barrier
	v_cndmask_b32_e64 v200, 0, 1, s[2:3]
	v_cmp_ne_u32_e64 s[4:5], 1, v200
	s_andn2_b64 vcc, exec, s[2:3]
	s_cbranch_vccnz .LBB0_1177
	ds_read_b128 v[180:183], v225 offset:16384
	ds_read_b128 v[196:199], v225 offset:17408
	ds_read_b128 v[176:179], v225 offset:18432
	ds_read_b128 v[192:195], v225 offset:19456
	ds_read_b128 v[172:175], v225 offset:20480
	ds_read_b128 v[188:191], v225 offset:21504
	ds_read_b128 v[168:171], v225 offset:22528
	ds_read_b128 v[184:187], v225 offset:23552
.LBB0_1177:
	s_add_u32 s56, s52, 0x80
	s_addc_u32 s57, s53, 0
	s_and_b64 s[54:55], s[54:55], exec
	s_cselect_b32 s55, s11, s81
	s_cselect_b32 s54, s41, s80
	s_mov_b32 m0, s61
	s_cselect_b32 s57, s23, s57
	s_cselect_b32 s56, s22, s56
	v_lshl_add_u64 v[204:205], s[54:55], 0, v[208:209]
	s_add_u32 s84, s54, 0x4000
	global_load_lds_dwordx4 v[204:205], off
	v_lshl_add_u64 v[204:205], s[54:55], 0, v[210:211]
	s_mov_b32 m0, s62
	s_addc_u32 s85, s55, 0
	global_load_lds_dwordx4 v[204:205], off
	v_lshl_add_u64 v[204:205], s[84:85], 0, v[208:209]
	s_mov_b32 m0, s63
	s_and_b64 vcc, exec, s[4:5]
	global_load_lds_dwordx4 v[204:205], off
	v_lshl_add_u64 v[204:205], s[84:85], 0, v[210:211]
	s_mov_b32 m0, s64
	s_nop 0
	global_load_lds_dwordx4 v[204:205], off
	s_mov_b32 m0, s9
	s_nop 0
	global_load_lds_dwordx4 v2, s[56:57]
	s_mov_b32 m0, s65
	s_nop 0
	global_load_lds_dwordx4 v212, s[56:57]
	s_waitcnt vmcnt(8)
	s_waitcnt lgkmcnt(0)
	s_barrier
	s_cbranch_vccnz .LBB0_1179
	s_waitcnt lgkmcnt(0)
	v_mfma_f32_16x16x32_bf16 v[64:67], v[152:155], v[180:183], v[64:67]
	v_mfma_f32_16x16x32_bf16 v[60:63], v[160:163], v[180:183], v[60:63]
	v_mfma_f32_16x16x32_bf16 v[56:59], v[152:155], v[176:179], v[56:59]
	v_mfma_f32_16x16x32_bf16 v[52:55], v[160:163], v[176:179], v[52:55]
	v_mfma_f32_16x16x32_bf16 v[48:51], v[152:155], v[172:175], v[48:51]
	v_mfma_f32_16x16x32_bf16 v[44:47], v[160:163], v[172:175], v[44:47]
	v_mfma_f32_16x16x32_bf16 v[40:43], v[152:155], v[168:171], v[40:43]
	v_mfma_f32_16x16x32_bf16 v[36:39], v[160:163], v[168:171], v[36:39]
	v_mfma_f32_16x16x32_bf16 v[64:67], v[156:159], v[196:199], v[64:67]
	v_mfma_f32_16x16x32_bf16 v[60:63], v[164:167], v[196:199], v[60:63]
	v_mfma_f32_16x16x32_bf16 v[56:59], v[156:159], v[192:195], v[56:59]
	v_mfma_f32_16x16x32_bf16 v[52:55], v[164:167], v[192:195], v[52:55]
	v_mfma_f32_16x16x32_bf16 v[48:51], v[156:159], v[188:191], v[48:51]
	v_mfma_f32_16x16x32_bf16 v[44:47], v[164:167], v[188:191], v[44:47]
	v_mfma_f32_16x16x32_bf16 v[40:43], v[156:159], v[184:187], v[40:43]
	v_mfma_f32_16x16x32_bf16 v[36:39], v[164:167], v[184:187], v[36:39]
	v_mfma_f32_16x16x32_bf16 v[32:35], v[136:139], v[180:183], v[32:35]
	v_mfma_f32_16x16x32_bf16 v[28:31], v[144:147], v[180:183], v[28:31]
	v_mfma_f32_16x16x32_bf16 v[24:27], v[136:139], v[176:179], v[24:27]
	v_mfma_f32_16x16x32_bf16 v[20:23], v[144:147], v[176:179], v[20:23]
	v_mfma_f32_16x16x32_bf16 v[16:19], v[136:139], v[172:175], v[16:19]
	v_mfma_f32_16x16x32_bf16 v[12:15], v[144:147], v[172:175], v[12:15]
	v_mfma_f32_16x16x32_bf16 v[8:11], v[136:139], v[168:171], v[8:11]
	v_mfma_f32_16x16x32_bf16 v[4:7], v[144:147], v[168:171], v[4:7]
	v_mfma_f32_16x16x32_bf16 v[32:35], v[140:143], v[196:199], v[32:35]
	v_mfma_f32_16x16x32_bf16 v[28:31], v[148:151], v[196:199], v[28:31]
	v_mfma_f32_16x16x32_bf16 v[24:27], v[140:143], v[192:195], v[24:27]
	v_mfma_f32_16x16x32_bf16 v[20:23], v[148:151], v[192:195], v[20:23]
	v_mfma_f32_16x16x32_bf16 v[16:19], v[140:143], v[188:191], v[16:19]
	v_mfma_f32_16x16x32_bf16 v[12:15], v[148:151], v[188:191], v[12:15]
	v_mfma_f32_16x16x32_bf16 v[8:11], v[140:143], v[184:187], v[8:11]
	v_mfma_f32_16x16x32_bf16 v[4:7], v[148:151], v[184:187], v[4:7]
.LBB0_1179:
	s_barrier
	v_add_u32_e32 v136, 0x18000, v224
	v_add_u32_e32 v148, 0x1c000, v224
	ds_read_b128 v[152:155], v136
	ds_read_b128 v[156:159], v136 offset:1024
	ds_read_b128 v[160:163], v136 offset:2048
	ds_read_b128 v[164:167], v136 offset:3072
	ds_read_b128 v[136:139], v148
	ds_read_b128 v[140:143], v148 offset:1024
	ds_read_b128 v[144:147], v148 offset:2048
	ds_read_b128 v[148:151], v148 offset:3072
	s_mov_b32 m0, s66
	s_waitcnt lgkmcnt(0)
	ds_read_b128 v[180:183], v225 offset:32768
	ds_read_b128 v[196:199], v225 offset:33792
	ds_read_b128 v[176:179], v225 offset:34816
	ds_read_b128 v[192:195], v225 offset:35840
	ds_read_b128 v[172:175], v225 offset:36864
	ds_read_b128 v[188:191], v225 offset:37888
	ds_read_b128 v[168:171], v225 offset:38912
	ds_read_b128 v[184:187], v225 offset:39936
	global_load_lds_dwordx4 v218, s[56:57]
	s_mov_b32 m0, s67
	s_nop 0
	global_load_lds_dwordx4 v220, s[56:57]
	s_waitcnt vmcnt(8)
	s_waitcnt lgkmcnt(0)
	s_barrier
	s_waitcnt lgkmcnt(0)
	v_mfma_f32_16x16x32_bf16 v[132:135], v[152:155], v[180:183], v[132:135]
	v_mfma_f32_16x16x32_bf16 v[128:131], v[160:163], v[180:183], v[128:131]
	v_mfma_f32_16x16x32_bf16 v[124:127], v[152:155], v[176:179], v[124:127]
	v_mfma_f32_16x16x32_bf16 v[120:123], v[160:163], v[176:179], v[120:123]
	v_mfma_f32_16x16x32_bf16 v[116:119], v[152:155], v[172:175], v[116:119]
	v_mfma_f32_16x16x32_bf16 v[112:115], v[160:163], v[172:175], v[112:115]
	v_mfma_f32_16x16x32_bf16 v[108:111], v[152:155], v[168:171], v[108:111]
	v_mfma_f32_16x16x32_bf16 v[104:107], v[160:163], v[168:171], v[104:107]
	v_mfma_f32_16x16x32_bf16 v[132:135], v[156:159], v[196:199], v[132:135]
	v_mfma_f32_16x16x32_bf16 v[128:131], v[164:167], v[196:199], v[128:131]
	v_mfma_f32_16x16x32_bf16 v[124:127], v[156:159], v[192:195], v[124:127]
	v_mfma_f32_16x16x32_bf16 v[120:123], v[164:167], v[192:195], v[120:123]
	v_mfma_f32_16x16x32_bf16 v[116:119], v[156:159], v[188:191], v[116:119]
	v_mfma_f32_16x16x32_bf16 v[112:115], v[164:167], v[188:191], v[112:115]
	v_mfma_f32_16x16x32_bf16 v[108:111], v[156:159], v[184:187], v[108:111]
	v_mfma_f32_16x16x32_bf16 v[104:107], v[164:167], v[184:187], v[104:107]
	v_mfma_f32_16x16x32_bf16 v[100:103], v[136:139], v[180:183], v[100:103]
	v_mfma_f32_16x16x32_bf16 v[96:99], v[144:147], v[180:183], v[96:99]
	v_mfma_f32_16x16x32_bf16 v[92:95], v[136:139], v[176:179], v[92:95]
	v_mfma_f32_16x16x32_bf16 v[88:91], v[144:147], v[176:179], v[88:91]
	v_mfma_f32_16x16x32_bf16 v[80:83], v[136:139], v[172:175], v[80:83]
	v_mfma_f32_16x16x32_bf16 v[76:79], v[144:147], v[172:175], v[76:79]
	v_mfma_f32_16x16x32_bf16 v[72:75], v[136:139], v[168:171], v[72:75]
	v_mfma_f32_16x16x32_bf16 v[68:71], v[144:147], v[168:171], v[68:71]
	v_mfma_f32_16x16x32_bf16 v[100:103], v[140:143], v[196:199], v[100:103]
	v_mfma_f32_16x16x32_bf16 v[96:99], v[148:151], v[196:199], v[96:99]
	v_mfma_f32_16x16x32_bf16 v[92:95], v[140:143], v[192:195], v[92:95]
	v_mfma_f32_16x16x32_bf16 v[88:91], v[148:151], v[192:195], v[88:91]
	v_mfma_f32_16x16x32_bf16 v[80:83], v[140:143], v[188:191], v[80:83]
	v_mfma_f32_16x16x32_bf16 v[76:79], v[148:151], v[188:191], v[76:79]
	v_mfma_f32_16x16x32_bf16 v[72:75], v[140:143], v[184:187], v[72:75]
	v_mfma_f32_16x16x32_bf16 v[68:71], v[148:151], v[184:187], v[68:71]
	s_barrier
	s_and_b64 vcc, exec, s[4:5]
	s_cbranch_vccnz .LBB0_1181
	ds_read_b128 v[180:183], v225 offset:49152
	ds_read_b128 v[196:199], v225 offset:50176
	ds_read_b128 v[176:179], v225 offset:51200
	ds_read_b128 v[192:195], v225 offset:52224
	ds_read_b128 v[172:175], v225 offset:53248
	ds_read_b128 v[188:191], v225 offset:54272
	ds_read_b128 v[168:171], v225 offset:55296
	ds_read_b128 v[184:187], v225 offset:56320
.LBB0_1181:
	v_mov_b32_e32 v213, v3
	v_lshl_add_u64 v[204:205], s[56:57], 0, v[2:3]
	v_lshl_add_u64 v[240:241], s[56:57], 0, v[212:213]
	s_add_u32 s56, s54, 0x8000
	s_addc_u32 s57, s55, 0
	s_mov_b32 m0, s69
	v_lshl_add_u64 v[242:243], s[56:57], 0, v[208:209]
	s_add_u32 s54, s54, 0xc000
	global_load_lds_dwordx4 v[242:243], off
	v_lshl_add_u64 v[242:243], s[56:57], 0, v[210:211]
	s_mov_b32 m0, s70
	s_addc_u32 s55, s55, 0
	global_load_lds_dwordx4 v[242:243], off
	v_lshl_add_u64 v[242:243], s[54:55], 0, v[208:209]
	s_mov_b32 m0, s73
	v_lshl_add_u64 v[204:205], v[204:205], 0, s[36:37]
	global_load_lds_dwordx4 v[242:243], off
	v_lshl_add_u64 v[242:243], s[54:55], 0, v[210:211]
	s_mov_b32 m0, s74
	s_and_b64 vcc, exec, s[4:5]
	global_load_lds_dwordx4 v[242:243], off
	s_mov_b32 m0, s71
	s_nop 0
	global_load_lds_dwordx4 v[204:205], off
	v_lshl_add_u64 v[204:205], v[240:241], 0, s[36:37]
	s_mov_b32 m0, s72
	s_nop 0
	global_load_lds_dwordx4 v[204:205], off
	s_waitcnt vmcnt(8)
	s_waitcnt lgkmcnt(0)
	s_barrier
	s_cbranch_vccnz .LBB0_1164
	s_waitcnt lgkmcnt(0)
	v_mfma_f32_16x16x32_bf16 v[64:67], v[152:155], v[180:183], v[64:67]
	v_mfma_f32_16x16x32_bf16 v[60:63], v[160:163], v[180:183], v[60:63]
	v_mfma_f32_16x16x32_bf16 v[56:59], v[152:155], v[176:179], v[56:59]
	v_mfma_f32_16x16x32_bf16 v[52:55], v[160:163], v[176:179], v[52:55]
	v_mfma_f32_16x16x32_bf16 v[48:51], v[152:155], v[172:175], v[48:51]
	v_mfma_f32_16x16x32_bf16 v[44:47], v[160:163], v[172:175], v[44:47]
	v_mfma_f32_16x16x32_bf16 v[40:43], v[152:155], v[168:171], v[40:43]
	v_mfma_f32_16x16x32_bf16 v[36:39], v[160:163], v[168:171], v[36:39]
	v_mfma_f32_16x16x32_bf16 v[64:67], v[156:159], v[196:199], v[64:67]
	v_mfma_f32_16x16x32_bf16 v[60:63], v[164:167], v[196:199], v[60:63]
	v_mfma_f32_16x16x32_bf16 v[56:59], v[156:159], v[192:195], v[56:59]
	v_mfma_f32_16x16x32_bf16 v[52:55], v[164:167], v[192:195], v[52:55]
	v_mfma_f32_16x16x32_bf16 v[48:51], v[156:159], v[188:191], v[48:51]
	v_mfma_f32_16x16x32_bf16 v[44:47], v[164:167], v[188:191], v[44:47]
	v_mfma_f32_16x16x32_bf16 v[40:43], v[156:159], v[184:187], v[40:43]
	v_mfma_f32_16x16x32_bf16 v[36:39], v[164:167], v[184:187], v[36:39]
	v_mfma_f32_16x16x32_bf16 v[32:35], v[136:139], v[180:183], v[32:35]
	v_mfma_f32_16x16x32_bf16 v[28:31], v[144:147], v[180:183], v[28:31]
	v_mfma_f32_16x16x32_bf16 v[24:27], v[136:139], v[176:179], v[24:27]
	v_mfma_f32_16x16x32_bf16 v[20:23], v[144:147], v[176:179], v[20:23]
	v_mfma_f32_16x16x32_bf16 v[16:19], v[136:139], v[172:175], v[16:19]
	v_mfma_f32_16x16x32_bf16 v[12:15], v[144:147], v[172:175], v[12:15]
	v_mfma_f32_16x16x32_bf16 v[8:11], v[136:139], v[168:171], v[8:11]
	v_mfma_f32_16x16x32_bf16 v[4:7], v[144:147], v[168:171], v[4:7]
	v_mfma_f32_16x16x32_bf16 v[32:35], v[140:143], v[196:199], v[32:35]
	v_mfma_f32_16x16x32_bf16 v[28:31], v[148:151], v[196:199], v[28:31]
	v_mfma_f32_16x16x32_bf16 v[24:27], v[140:143], v[192:195], v[24:27]
	v_mfma_f32_16x16x32_bf16 v[20:23], v[148:151], v[192:195], v[20:23]
	v_mfma_f32_16x16x32_bf16 v[16:19], v[140:143], v[188:191], v[16:19]
	v_mfma_f32_16x16x32_bf16 v[12:15], v[148:151], v[188:191], v[12:15]
	v_mfma_f32_16x16x32_bf16 v[8:11], v[140:143], v[184:187], v[8:11]
	v_mfma_f32_16x16x32_bf16 v[4:7], v[148:151], v[184:187], v[4:7]
	s_branch .LBB0_1164

.LBB0_1311:
	s_waitcnt vmcnt(8)
	s_waitcnt lgkmcnt(0)
	s_barrier
	s_waitcnt lgkmcnt(0)
	v_mfma_f32_16x16x32_bf16 v[132:135], v[152:155], v[180:183], v[132:135]
	v_mfma_f32_16x16x32_bf16 v[128:131], v[160:163], v[180:183], v[128:131]
	v_mfma_f32_16x16x32_bf16 v[124:127], v[152:155], v[176:179], v[124:127]
	v_mfma_f32_16x16x32_bf16 v[120:123], v[160:163], v[176:179], v[120:123]
	v_mfma_f32_16x16x32_bf16 v[116:119], v[152:155], v[172:175], v[116:119]
	v_mfma_f32_16x16x32_bf16 v[112:115], v[160:163], v[172:175], v[112:115]
	v_mfma_f32_16x16x32_bf16 v[108:111], v[152:155], v[168:171], v[108:111]
	v_mfma_f32_16x16x32_bf16 v[104:107], v[160:163], v[168:171], v[104:107]
	v_mfma_f32_16x16x32_bf16 v[132:135], v[156:159], v[196:199], v[132:135]
	v_mfma_f32_16x16x32_bf16 v[128:131], v[164:167], v[196:199], v[128:131]
	v_mfma_f32_16x16x32_bf16 v[124:127], v[156:159], v[192:195], v[124:127]
	v_mfma_f32_16x16x32_bf16 v[120:123], v[164:167], v[192:195], v[120:123]
	v_mfma_f32_16x16x32_bf16 v[116:119], v[156:159], v[188:191], v[116:119]
	v_mfma_f32_16x16x32_bf16 v[112:115], v[164:167], v[188:191], v[112:115]
	v_mfma_f32_16x16x32_bf16 v[108:111], v[156:159], v[184:187], v[108:111]
	v_mfma_f32_16x16x32_bf16 v[104:107], v[164:167], v[184:187], v[104:107]
	v_mfma_f32_16x16x32_bf16 v[100:103], v[136:139], v[180:183], v[100:103]
	v_mfma_f32_16x16x32_bf16 v[96:99], v[144:147], v[180:183], v[96:99]
	v_mfma_f32_16x16x32_bf16 v[92:95], v[136:139], v[176:179], v[92:95]
	v_mfma_f32_16x16x32_bf16 v[88:91], v[144:147], v[176:179], v[88:91]
	v_mfma_f32_16x16x32_bf16 v[80:83], v[136:139], v[172:175], v[80:83]
	v_mfma_f32_16x16x32_bf16 v[76:79], v[144:147], v[172:175], v[76:79]
	v_mfma_f32_16x16x32_bf16 v[72:75], v[136:139], v[168:171], v[72:75]
	v_mfma_f32_16x16x32_bf16 v[68:71], v[144:147], v[168:171], v[68:71]
	v_mfma_f32_16x16x32_bf16 v[100:103], v[140:143], v[196:199], v[100:103]
	v_mfma_f32_16x16x32_bf16 v[96:99], v[148:151], v[196:199], v[96:99]
	v_mfma_f32_16x16x32_bf16 v[92:95], v[140:143], v[192:195], v[92:95]
	v_mfma_f32_16x16x32_bf16 v[88:91], v[148:151], v[192:195], v[88:91]
	v_mfma_f32_16x16x32_bf16 v[80:83], v[140:143], v[188:191], v[80:83]
	v_mfma_f32_16x16x32_bf16 v[76:79], v[148:151], v[188:191], v[76:79]
	v_mfma_f32_16x16x32_bf16 v[72:75], v[140:143], v[184:187], v[72:75]
	v_mfma_f32_16x16x32_bf16 v[68:71], v[148:151], v[184:187], v[68:71]
	s_barrier
	v_cndmask_b32_e64 v200, 0, 1, s[2:3]
	v_cmp_ne_u32_e64 s[4:5], 1, v200
	s_andn2_b64 vcc, exec, s[2:3]
	s_cbranch_vccnz .LBB0_1313
	ds_read_b128 v[180:183], v242 offset:16384
	ds_read_b128 v[196:199], v242 offset:17408
	ds_read_b128 v[176:179], v242 offset:18432
	ds_read_b128 v[192:195], v242 offset:19456
	ds_read_b128 v[172:175], v242 offset:20480
	ds_read_b128 v[188:191], v242 offset:21504
	ds_read_b128 v[168:171], v242 offset:22528
	ds_read_b128 v[184:187], v242 offset:23552
.LBB0_1313:
	s_add_u32 s56, s52, 0x80
	s_addc_u32 s57, s53, 0
	s_and_b64 s[54:55], s[54:55], exec
	s_cselect_b32 s55, s41, s83
	s_cselect_b32 s54, s43, s82
	s_mov_b32 m0, s65
	s_cselect_b32 s57, s25, s57
	s_cselect_b32 s56, s24, s56
	v_lshl_add_u64 v[204:205], s[54:55], 0, v[208:209]
	s_add_u32 s86, s54, 0x4000
	global_load_lds_dwordx4 v[204:205], off
	v_lshl_add_u64 v[204:205], s[54:55], 0, v[210:211]
	s_mov_b32 m0, s66
	s_addc_u32 s87, s55, 0
	global_load_lds_dwordx4 v[204:205], off
	v_lshl_add_u64 v[204:205], s[86:87], 0, v[208:209]
	s_mov_b32 m0, s67
	s_and_b64 vcc, exec, s[4:5]
	global_load_lds_dwordx4 v[204:205], off
	v_lshl_add_u64 v[204:205], s[86:87], 0, v[210:211]
	s_mov_b32 m0, s68
	s_nop 0
	global_load_lds_dwordx4 v[204:205], off
	s_mov_b32 m0, s11
	s_nop 0
	global_load_lds_dwordx4 v2, s[56:57]
	s_mov_b32 m0, s69
	s_nop 0
	global_load_lds_dwordx4 v212, s[56:57]
	s_waitcnt vmcnt(8)
	s_waitcnt lgkmcnt(0)
	s_barrier
	s_cbranch_vccnz .LBB0_1315
	s_waitcnt lgkmcnt(0)
	v_mfma_f32_16x16x32_bf16 v[64:67], v[152:155], v[180:183], v[64:67]
	v_mfma_f32_16x16x32_bf16 v[60:63], v[160:163], v[180:183], v[60:63]
	v_mfma_f32_16x16x32_bf16 v[56:59], v[152:155], v[176:179], v[56:59]
	v_mfma_f32_16x16x32_bf16 v[52:55], v[160:163], v[176:179], v[52:55]
	v_mfma_f32_16x16x32_bf16 v[48:51], v[152:155], v[172:175], v[48:51]
	v_mfma_f32_16x16x32_bf16 v[44:47], v[160:163], v[172:175], v[44:47]
	v_mfma_f32_16x16x32_bf16 v[40:43], v[152:155], v[168:171], v[40:43]
	v_mfma_f32_16x16x32_bf16 v[36:39], v[160:163], v[168:171], v[36:39]
	v_mfma_f32_16x16x32_bf16 v[64:67], v[156:159], v[196:199], v[64:67]
	v_mfma_f32_16x16x32_bf16 v[60:63], v[164:167], v[196:199], v[60:63]
	v_mfma_f32_16x16x32_bf16 v[56:59], v[156:159], v[192:195], v[56:59]
	v_mfma_f32_16x16x32_bf16 v[52:55], v[164:167], v[192:195], v[52:55]
	v_mfma_f32_16x16x32_bf16 v[48:51], v[156:159], v[188:191], v[48:51]
	v_mfma_f32_16x16x32_bf16 v[44:47], v[164:167], v[188:191], v[44:47]
	v_mfma_f32_16x16x32_bf16 v[40:43], v[156:159], v[184:187], v[40:43]
	v_mfma_f32_16x16x32_bf16 v[36:39], v[164:167], v[184:187], v[36:39]
	v_mfma_f32_16x16x32_bf16 v[32:35], v[136:139], v[180:183], v[32:35]
	v_mfma_f32_16x16x32_bf16 v[28:31], v[144:147], v[180:183], v[28:31]
	v_mfma_f32_16x16x32_bf16 v[24:27], v[136:139], v[176:179], v[24:27]
	v_mfma_f32_16x16x32_bf16 v[20:23], v[144:147], v[176:179], v[20:23]
	v_mfma_f32_16x16x32_bf16 v[16:19], v[136:139], v[172:175], v[16:19]
	v_mfma_f32_16x16x32_bf16 v[12:15], v[144:147], v[172:175], v[12:15]
	v_mfma_f32_16x16x32_bf16 v[8:11], v[136:139], v[168:171], v[8:11]
	v_mfma_f32_16x16x32_bf16 v[4:7], v[144:147], v[168:171], v[4:7]
	v_mfma_f32_16x16x32_bf16 v[32:35], v[140:143], v[196:199], v[32:35]
	v_mfma_f32_16x16x32_bf16 v[28:31], v[148:151], v[196:199], v[28:31]
	v_mfma_f32_16x16x32_bf16 v[24:27], v[140:143], v[192:195], v[24:27]
	v_mfma_f32_16x16x32_bf16 v[20:23], v[148:151], v[192:195], v[20:23]
	v_mfma_f32_16x16x32_bf16 v[16:19], v[140:143], v[188:191], v[16:19]
	v_mfma_f32_16x16x32_bf16 v[12:15], v[148:151], v[188:191], v[12:15]
	v_mfma_f32_16x16x32_bf16 v[8:11], v[140:143], v[184:187], v[8:11]
	v_mfma_f32_16x16x32_bf16 v[4:7], v[148:151], v[184:187], v[4:7]
.LBB0_1315:
	s_barrier
	v_add_u32_e32 v136, 0x18000, v241
	v_add_u32_e32 v148, 0x1c000, v241
	ds_read_b128 v[152:155], v136
	ds_read_b128 v[156:159], v136 offset:1024
	ds_read_b128 v[160:163], v136 offset:2048
	ds_read_b128 v[164:167], v136 offset:3072
	ds_read_b128 v[136:139], v148
	ds_read_b128 v[140:143], v148 offset:1024
	ds_read_b128 v[144:147], v148 offset:2048
	ds_read_b128 v[148:151], v148 offset:3072
	s_mov_b32 m0, s70
	s_waitcnt lgkmcnt(0)
	ds_read_b128 v[180:183], v242 offset:32768
	ds_read_b128 v[196:199], v242 offset:33792
	ds_read_b128 v[176:179], v242 offset:34816
	ds_read_b128 v[192:195], v242 offset:35840
	ds_read_b128 v[172:175], v242 offset:36864
	ds_read_b128 v[188:191], v242 offset:37888
	ds_read_b128 v[168:171], v242 offset:38912
	ds_read_b128 v[184:187], v242 offset:39936
	global_load_lds_dwordx4 v218, s[56:57]
	s_mov_b32 m0, s71
	s_nop 0
	global_load_lds_dwordx4 v219, s[56:57]
	s_waitcnt vmcnt(8)
	s_waitcnt lgkmcnt(0)
	s_barrier
	s_waitcnt lgkmcnt(0)
	v_mfma_f32_16x16x32_bf16 v[132:135], v[152:155], v[180:183], v[132:135]
	v_mfma_f32_16x16x32_bf16 v[128:131], v[160:163], v[180:183], v[128:131]
	v_mfma_f32_16x16x32_bf16 v[124:127], v[152:155], v[176:179], v[124:127]
	v_mfma_f32_16x16x32_bf16 v[120:123], v[160:163], v[176:179], v[120:123]
	v_mfma_f32_16x16x32_bf16 v[116:119], v[152:155], v[172:175], v[116:119]
	v_mfma_f32_16x16x32_bf16 v[112:115], v[160:163], v[172:175], v[112:115]
	v_mfma_f32_16x16x32_bf16 v[108:111], v[152:155], v[168:171], v[108:111]
	v_mfma_f32_16x16x32_bf16 v[104:107], v[160:163], v[168:171], v[104:107]
	v_mfma_f32_16x16x32_bf16 v[132:135], v[156:159], v[196:199], v[132:135]
	v_mfma_f32_16x16x32_bf16 v[128:131], v[164:167], v[196:199], v[128:131]
	v_mfma_f32_16x16x32_bf16 v[124:127], v[156:159], v[192:195], v[124:127]
	v_mfma_f32_16x16x32_bf16 v[120:123], v[164:167], v[192:195], v[120:123]
	v_mfma_f32_16x16x32_bf16 v[116:119], v[156:159], v[188:191], v[116:119]
	v_mfma_f32_16x16x32_bf16 v[112:115], v[164:167], v[188:191], v[112:115]
	v_mfma_f32_16x16x32_bf16 v[108:111], v[156:159], v[184:187], v[108:111]
	v_mfma_f32_16x16x32_bf16 v[104:107], v[164:167], v[184:187], v[104:107]
	v_mfma_f32_16x16x32_bf16 v[100:103], v[136:139], v[180:183], v[100:103]
	v_mfma_f32_16x16x32_bf16 v[96:99], v[144:147], v[180:183], v[96:99]
	v_mfma_f32_16x16x32_bf16 v[92:95], v[136:139], v[176:179], v[92:95]
	v_mfma_f32_16x16x32_bf16 v[88:91], v[144:147], v[176:179], v[88:91]
	v_mfma_f32_16x16x32_bf16 v[80:83], v[136:139], v[172:175], v[80:83]
	v_mfma_f32_16x16x32_bf16 v[76:79], v[144:147], v[172:175], v[76:79]
	v_mfma_f32_16x16x32_bf16 v[72:75], v[136:139], v[168:171], v[72:75]
	v_mfma_f32_16x16x32_bf16 v[68:71], v[144:147], v[168:171], v[68:71]
	v_mfma_f32_16x16x32_bf16 v[100:103], v[140:143], v[196:199], v[100:103]
	v_mfma_f32_16x16x32_bf16 v[96:99], v[148:151], v[196:199], v[96:99]
	v_mfma_f32_16x16x32_bf16 v[92:95], v[140:143], v[192:195], v[92:95]
	v_mfma_f32_16x16x32_bf16 v[88:91], v[148:151], v[192:195], v[88:91]
	v_mfma_f32_16x16x32_bf16 v[80:83], v[140:143], v[188:191], v[80:83]
	v_mfma_f32_16x16x32_bf16 v[76:79], v[148:151], v[188:191], v[76:79]
	v_mfma_f32_16x16x32_bf16 v[72:75], v[140:143], v[184:187], v[72:75]
	v_mfma_f32_16x16x32_bf16 v[68:71], v[148:151], v[184:187], v[68:71]
	s_barrier
	s_and_b64 vcc, exec, s[4:5]
	s_cbranch_vccnz .LBB0_1317
	ds_read_b128 v[180:183], v242 offset:49152
	ds_read_b128 v[196:199], v242 offset:50176
	ds_read_b128 v[176:179], v242 offset:51200
	ds_read_b128 v[192:195], v242 offset:52224
	ds_read_b128 v[172:175], v242 offset:53248
	ds_read_b128 v[188:191], v242 offset:54272
	ds_read_b128 v[168:171], v242 offset:55296
	ds_read_b128 v[184:187], v242 offset:56320
.LBB0_1317:
	v_mov_b32_e32 v213, v3
	v_lshl_add_u64 v[204:205], s[56:57], 0, v[2:3]
	v_lshl_add_u64 v[206:207], s[56:57], 0, v[212:213]
	s_add_u32 s56, s54, 0x8000
	s_addc_u32 s57, s55, 0
	s_mov_b32 m0, s72
	v_lshl_add_u64 v[200:201], s[56:57], 0, v[208:209]
	s_add_u32 s54, s54, 0xc000
	global_load_lds_dwordx4 v[200:201], off
	v_lshl_add_u64 v[200:201], s[56:57], 0, v[210:211]
	s_mov_b32 m0, s73
	s_addc_u32 s55, s55, 0
	global_load_lds_dwordx4 v[200:201], off
	v_lshl_add_u64 v[200:201], s[54:55], 0, v[208:209]
	s_mov_b32 m0, s76
	s_and_b64 vcc, exec, s[4:5]
	global_load_lds_dwordx4 v[200:201], off
	v_lshl_add_u64 v[200:201], s[54:55], 0, v[210:211]
	s_mov_b32 m0, s77
	s_nop 0
	global_load_lds_dwordx4 v[200:201], off
	v_lshl_add_u64 v[200:201], v[204:205], 0, s[36:37]
	s_mov_b32 m0, s74
	s_nop 0
	global_load_lds_dwordx4 v[200:201], off
	v_lshl_add_u64 v[200:201], v[206:207], 0, s[36:37]
	s_mov_b32 m0, s75
	s_nop 0
	global_load_lds_dwordx4 v[200:201], off
	s_waitcnt vmcnt(8)
	s_waitcnt lgkmcnt(0)
	s_barrier
	s_cbranch_vccnz .LBB0_1308
	s_waitcnt lgkmcnt(0)
	v_mfma_f32_16x16x32_bf16 v[64:67], v[152:155], v[180:183], v[64:67]
	v_mfma_f32_16x16x32_bf16 v[60:63], v[160:163], v[180:183], v[60:63]
	v_mfma_f32_16x16x32_bf16 v[56:59], v[152:155], v[176:179], v[56:59]
	v_mfma_f32_16x16x32_bf16 v[52:55], v[160:163], v[176:179], v[52:55]
	v_mfma_f32_16x16x32_bf16 v[48:51], v[152:155], v[172:175], v[48:51]
	v_mfma_f32_16x16x32_bf16 v[44:47], v[160:163], v[172:175], v[44:47]
	v_mfma_f32_16x16x32_bf16 v[40:43], v[152:155], v[168:171], v[40:43]
	v_mfma_f32_16x16x32_bf16 v[36:39], v[160:163], v[168:171], v[36:39]
	v_mfma_f32_16x16x32_bf16 v[64:67], v[156:159], v[196:199], v[64:67]
	v_mfma_f32_16x16x32_bf16 v[60:63], v[164:167], v[196:199], v[60:63]
	v_mfma_f32_16x16x32_bf16 v[56:59], v[156:159], v[192:195], v[56:59]
	v_mfma_f32_16x16x32_bf16 v[52:55], v[164:167], v[192:195], v[52:55]
	v_mfma_f32_16x16x32_bf16 v[48:51], v[156:159], v[188:191], v[48:51]
	v_mfma_f32_16x16x32_bf16 v[44:47], v[164:167], v[188:191], v[44:47]
	v_mfma_f32_16x16x32_bf16 v[40:43], v[156:159], v[184:187], v[40:43]
	v_mfma_f32_16x16x32_bf16 v[36:39], v[164:167], v[184:187], v[36:39]
	v_mfma_f32_16x16x32_bf16 v[32:35], v[136:139], v[180:183], v[32:35]
	v_mfma_f32_16x16x32_bf16 v[28:31], v[144:147], v[180:183], v[28:31]
	v_mfma_f32_16x16x32_bf16 v[24:27], v[136:139], v[176:179], v[24:27]
	v_mfma_f32_16x16x32_bf16 v[20:23], v[144:147], v[176:179], v[20:23]
	v_mfma_f32_16x16x32_bf16 v[16:19], v[136:139], v[172:175], v[16:19]
	v_mfma_f32_16x16x32_bf16 v[12:15], v[144:147], v[172:175], v[12:15]
	v_mfma_f32_16x16x32_bf16 v[8:11], v[136:139], v[168:171], v[8:11]
	v_mfma_f32_16x16x32_bf16 v[4:7], v[144:147], v[168:171], v[4:7]
	v_mfma_f32_16x16x32_bf16 v[32:35], v[140:143], v[196:199], v[32:35]
	v_mfma_f32_16x16x32_bf16 v[28:31], v[148:151], v[196:199], v[28:31]
	v_mfma_f32_16x16x32_bf16 v[24:27], v[140:143], v[192:195], v[24:27]
	v_mfma_f32_16x16x32_bf16 v[20:23], v[148:151], v[192:195], v[20:23]
	v_mfma_f32_16x16x32_bf16 v[16:19], v[140:143], v[188:191], v[16:19]
	v_mfma_f32_16x16x32_bf16 v[12:15], v[148:151], v[188:191], v[12:15]
	v_mfma_f32_16x16x32_bf16 v[8:11], v[140:143], v[184:187], v[8:11]
	v_mfma_f32_16x16x32_bf16 v[4:7], v[148:151], v[184:187], v[4:7]
	s_branch .LBB0_1308

.LBB0_1429:
	s_add_u32 s52, s48, 0x80
	s_addc_u32 s53, s49, 0
	s_and_b64 s[50:51], s[50:51], exec
	s_cselect_b32 s51, s15, s74
	s_cselect_b32 s50, s39, s73
	s_mov_b32 m0, s55
	s_cselect_b32 s53, s25, s53
	s_cselect_b32 s52, s24, s52
	v_lshl_add_u64 v[200:201], s[50:51], 0, v[208:209]
	s_add_u32 s76, s50, 0x4000
	global_load_lds_dwordx4 v[200:201], off
	v_lshl_add_u64 v[200:201], s[50:51], 0, v[210:211]
	s_mov_b32 m0, s56
	s_addc_u32 s77, s51, 0
	global_load_lds_dwordx4 v[200:201], off
	v_lshl_add_u64 v[200:201], s[76:77], 0, v[208:209]
	s_mov_b32 m0, s57
	s_and_b64 vcc, exec, s[4:5]
	global_load_lds_dwordx4 v[200:201], off
	v_lshl_add_u64 v[200:201], s[76:77], 0, v[210:211]
	s_mov_b32 m0, s59
	s_nop 0
	global_load_lds_dwordx4 v[200:201], off
	s_mov_b32 m0, s7
	s_nop 0
	global_load_lds_dwordx4 v2, s[52:53]
	s_mov_b32 m0, s60
	s_nop 0
	global_load_lds_dwordx4 v212, s[52:53]
	s_waitcnt vmcnt(8)
	s_waitcnt lgkmcnt(0)
	s_barrier
	s_cbranch_vccnz .LBB0_1431
	s_waitcnt lgkmcnt(0)
	v_mfma_f32_16x16x32_bf16 v[64:67], v[152:155], v[180:183], v[64:67]
	v_mfma_f32_16x16x32_bf16 v[60:63], v[160:163], v[180:183], v[60:63]
	v_mfma_f32_16x16x32_bf16 v[56:59], v[152:155], v[176:179], v[56:59]
	v_mfma_f32_16x16x32_bf16 v[52:55], v[160:163], v[176:179], v[52:55]
	v_mfma_f32_16x16x32_bf16 v[48:51], v[152:155], v[172:175], v[48:51]
	v_mfma_f32_16x16x32_bf16 v[44:47], v[160:163], v[172:175], v[44:47]
	v_mfma_f32_16x16x32_bf16 v[40:43], v[152:155], v[168:171], v[40:43]
	v_mfma_f32_16x16x32_bf16 v[36:39], v[160:163], v[168:171], v[36:39]
	v_mfma_f32_16x16x32_bf16 v[64:67], v[156:159], v[196:199], v[64:67]
	v_mfma_f32_16x16x32_bf16 v[60:63], v[164:167], v[196:199], v[60:63]
	v_mfma_f32_16x16x32_bf16 v[56:59], v[156:159], v[192:195], v[56:59]
	v_mfma_f32_16x16x32_bf16 v[52:55], v[164:167], v[192:195], v[52:55]
	v_mfma_f32_16x16x32_bf16 v[48:51], v[156:159], v[188:191], v[48:51]
	v_mfma_f32_16x16x32_bf16 v[44:47], v[164:167], v[188:191], v[44:47]
	v_mfma_f32_16x16x32_bf16 v[40:43], v[156:159], v[184:187], v[40:43]
	v_mfma_f32_16x16x32_bf16 v[36:39], v[164:167], v[184:187], v[36:39]
	v_mfma_f32_16x16x32_bf16 v[32:35], v[136:139], v[180:183], v[32:35]
	v_mfma_f32_16x16x32_bf16 v[28:31], v[144:147], v[180:183], v[28:31]
	v_mfma_f32_16x16x32_bf16 v[24:27], v[136:139], v[176:179], v[24:27]
	v_mfma_f32_16x16x32_bf16 v[20:23], v[144:147], v[176:179], v[20:23]
	v_mfma_f32_16x16x32_bf16 v[16:19], v[136:139], v[172:175], v[16:19]
	v_mfma_f32_16x16x32_bf16 v[12:15], v[144:147], v[172:175], v[12:15]
	v_mfma_f32_16x16x32_bf16 v[8:11], v[136:139], v[168:171], v[8:11]
	v_mfma_f32_16x16x32_bf16 v[4:7], v[144:147], v[168:171], v[4:7]
	v_mfma_f32_16x16x32_bf16 v[32:35], v[140:143], v[196:199], v[32:35]
	v_mfma_f32_16x16x32_bf16 v[28:31], v[148:151], v[196:199], v[28:31]
	v_mfma_f32_16x16x32_bf16 v[24:27], v[140:143], v[192:195], v[24:27]
	v_mfma_f32_16x16x32_bf16 v[20:23], v[148:151], v[192:195], v[20:23]
	v_mfma_f32_16x16x32_bf16 v[16:19], v[140:143], v[188:191], v[16:19]
	v_mfma_f32_16x16x32_bf16 v[12:15], v[148:151], v[188:191], v[12:15]
	v_mfma_f32_16x16x32_bf16 v[8:11], v[140:143], v[184:187], v[8:11]
	v_mfma_f32_16x16x32_bf16 v[4:7], v[148:151], v[184:187], v[4:7]
.LBB0_1431:
	s_barrier
	v_add_u32_e32 v136, 0x18000, v241
	v_add_u32_e32 v148, 0x1c000, v241
	ds_read_b128 v[152:155], v136
	ds_read_b128 v[156:159], v136 offset:1024
	ds_read_b128 v[160:163], v136 offset:2048
	ds_read_b128 v[164:167], v136 offset:3072
	ds_read_b128 v[136:139], v148
	ds_read_b128 v[140:143], v148 offset:1024
	ds_read_b128 v[144:147], v148 offset:2048
	ds_read_b128 v[148:151], v148 offset:3072
	s_mov_b32 m0, s61
	s_waitcnt lgkmcnt(0)
	ds_read_b128 v[180:183], v242 offset:32768
	ds_read_b128 v[196:199], v242 offset:33792
	ds_read_b128 v[176:179], v242 offset:34816
	ds_read_b128 v[192:195], v242 offset:35840
	ds_read_b128 v[172:175], v242 offset:36864
	ds_read_b128 v[188:191], v242 offset:37888
	ds_read_b128 v[168:171], v242 offset:38912
	ds_read_b128 v[184:187], v242 offset:39936
	global_load_lds_dwordx4 v218, s[52:53]
	s_mov_b32 m0, s62
	s_nop 0
	global_load_lds_dwordx4 v219, s[52:53]
	s_waitcnt vmcnt(8)
	s_waitcnt lgkmcnt(0)
	s_barrier
	s_waitcnt lgkmcnt(0)
	v_mfma_f32_16x16x32_bf16 v[132:135], v[152:155], v[180:183], v[132:135]
	v_mfma_f32_16x16x32_bf16 v[128:131], v[160:163], v[180:183], v[128:131]
	v_mfma_f32_16x16x32_bf16 v[124:127], v[152:155], v[176:179], v[124:127]
	v_mfma_f32_16x16x32_bf16 v[120:123], v[160:163], v[176:179], v[120:123]
	v_mfma_f32_16x16x32_bf16 v[116:119], v[152:155], v[172:175], v[116:119]
	v_mfma_f32_16x16x32_bf16 v[112:115], v[160:163], v[172:175], v[112:115]
	v_mfma_f32_16x16x32_bf16 v[108:111], v[152:155], v[168:171], v[108:111]
	v_mfma_f32_16x16x32_bf16 v[104:107], v[160:163], v[168:171], v[104:107]
	v_mfma_f32_16x16x32_bf16 v[132:135], v[156:159], v[196:199], v[132:135]
	v_mfma_f32_16x16x32_bf16 v[128:131], v[164:167], v[196:199], v[128:131]
	v_mfma_f32_16x16x32_bf16 v[124:127], v[156:159], v[192:195], v[124:127]
	v_mfma_f32_16x16x32_bf16 v[120:123], v[164:167], v[192:195], v[120:123]
	v_mfma_f32_16x16x32_bf16 v[116:119], v[156:159], v[188:191], v[116:119]
	v_mfma_f32_16x16x32_bf16 v[112:115], v[164:167], v[188:191], v[112:115]
	v_mfma_f32_16x16x32_bf16 v[108:111], v[156:159], v[184:187], v[108:111]
	v_mfma_f32_16x16x32_bf16 v[104:107], v[164:167], v[184:187], v[104:107]
	v_mfma_f32_16x16x32_bf16 v[100:103], v[136:139], v[180:183], v[100:103]
	v_mfma_f32_16x16x32_bf16 v[96:99], v[144:147], v[180:183], v[96:99]
	v_mfma_f32_16x16x32_bf16 v[92:95], v[136:139], v[176:179], v[92:95]
	v_mfma_f32_16x16x32_bf16 v[88:91], v[144:147], v[176:179], v[88:91]
	v_mfma_f32_16x16x32_bf16 v[80:83], v[136:139], v[172:175], v[80:83]
	v_mfma_f32_16x16x32_bf16 v[76:79], v[144:147], v[172:175], v[76:79]
	v_mfma_f32_16x16x32_bf16 v[72:75], v[136:139], v[168:171], v[72:75]
	v_mfma_f32_16x16x32_bf16 v[68:71], v[144:147], v[168:171], v[68:71]
	v_mfma_f32_16x16x32_bf16 v[100:103], v[140:143], v[196:199], v[100:103]
	v_mfma_f32_16x16x32_bf16 v[96:99], v[148:151], v[196:199], v[96:99]
	v_mfma_f32_16x16x32_bf16 v[92:95], v[140:143], v[192:195], v[92:95]
	v_mfma_f32_16x16x32_bf16 v[88:91], v[148:151], v[192:195], v[88:91]
	v_mfma_f32_16x16x32_bf16 v[80:83], v[140:143], v[188:191], v[80:83]
	v_mfma_f32_16x16x32_bf16 v[76:79], v[148:151], v[188:191], v[76:79]
	v_mfma_f32_16x16x32_bf16 v[72:75], v[140:143], v[184:187], v[72:75]
	v_mfma_f32_16x16x32_bf16 v[68:71], v[148:151], v[184:187], v[68:71]
	s_barrier
	s_and_b64 vcc, exec, s[4:5]
	s_cbranch_vccnz .LBB0_1433
	ds_read_b128 v[180:183], v242 offset:49152
	ds_read_b128 v[196:199], v242 offset:50176
	ds_read_b128 v[176:179], v242 offset:51200
	ds_read_b128 v[192:195], v242 offset:52224
	ds_read_b128 v[172:175], v242 offset:53248
	ds_read_b128 v[188:191], v242 offset:54272
	ds_read_b128 v[168:171], v242 offset:55296
	ds_read_b128 v[184:187], v242 offset:56320
.LBB0_1433:
	v_mov_b32_e32 v213, v3
	v_lshl_add_u64 v[200:201], s[52:53], 0, v[2:3]
	v_lshl_add_u64 v[204:205], s[52:53], 0, v[212:213]
	s_add_u32 s52, s50, 0x8000
	s_addc_u32 s53, s51, 0
	s_mov_b32 m0, s63
	v_lshl_add_u64 v[206:207], s[52:53], 0, v[208:209]
	s_add_u32 s50, s50, 0xc000
	global_load_lds_dwordx4 v[206:207], off
	v_lshl_add_u64 v[206:207], s[52:53], 0, v[210:211]
	s_mov_b32 m0, s64
	s_addc_u32 s51, s51, 0
	global_load_lds_dwordx4 v[206:207], off
	v_lshl_add_u64 v[206:207], s[50:51], 0, v[208:209]
	s_mov_b32 m0, s67
	v_lshl_add_u64 v[200:201], v[200:201], 0, s[36:37]
	global_load_lds_dwordx4 v[206:207], off
	v_lshl_add_u64 v[206:207], s[50:51], 0, v[210:211]
	s_mov_b32 m0, s68
	s_and_b64 vcc, exec, s[4:5]
	global_load_lds_dwordx4 v[206:207], off
	s_mov_b32 m0, s65
	s_nop 0
	global_load_lds_dwordx4 v[200:201], off
	v_lshl_add_u64 v[200:201], v[204:205], 0, s[36:37]
	s_mov_b32 m0, s66
	s_nop 0
	global_load_lds_dwordx4 v[200:201], off
	s_waitcnt vmcnt(8)
	s_waitcnt lgkmcnt(0)
	s_barrier
	s_cbranch_vccnz .LBB0_1424
	s_waitcnt lgkmcnt(0)
	v_mfma_f32_16x16x32_bf16 v[64:67], v[152:155], v[180:183], v[64:67]
	v_mfma_f32_16x16x32_bf16 v[60:63], v[160:163], v[180:183], v[60:63]
	v_mfma_f32_16x16x32_bf16 v[56:59], v[152:155], v[176:179], v[56:59]
	v_mfma_f32_16x16x32_bf16 v[52:55], v[160:163], v[176:179], v[52:55]
	v_mfma_f32_16x16x32_bf16 v[48:51], v[152:155], v[172:175], v[48:51]
	v_mfma_f32_16x16x32_bf16 v[44:47], v[160:163], v[172:175], v[44:47]
	v_mfma_f32_16x16x32_bf16 v[40:43], v[152:155], v[168:171], v[40:43]
	v_mfma_f32_16x16x32_bf16 v[36:39], v[160:163], v[168:171], v[36:39]
	v_mfma_f32_16x16x32_bf16 v[64:67], v[156:159], v[196:199], v[64:67]
	v_mfma_f32_16x16x32_bf16 v[60:63], v[164:167], v[196:199], v[60:63]
	v_mfma_f32_16x16x32_bf16 v[56:59], v[156:159], v[192:195], v[56:59]
	v_mfma_f32_16x16x32_bf16 v[52:55], v[164:167], v[192:195], v[52:55]
	v_mfma_f32_16x16x32_bf16 v[48:51], v[156:159], v[188:191], v[48:51]
	v_mfma_f32_16x16x32_bf16 v[44:47], v[164:167], v[188:191], v[44:47]
	v_mfma_f32_16x16x32_bf16 v[40:43], v[156:159], v[184:187], v[40:43]
	v_mfma_f32_16x16x32_bf16 v[36:39], v[164:167], v[184:187], v[36:39]
	v_mfma_f32_16x16x32_bf16 v[32:35], v[136:139], v[180:183], v[32:35]
	v_mfma_f32_16x16x32_bf16 v[28:31], v[144:147], v[180:183], v[28:31]
	v_mfma_f32_16x16x32_bf16 v[24:27], v[136:139], v[176:179], v[24:27]
	v_mfma_f32_16x16x32_bf16 v[20:23], v[144:147], v[176:179], v[20:23]
	v_mfma_f32_16x16x32_bf16 v[16:19], v[136:139], v[172:175], v[16:19]
	v_mfma_f32_16x16x32_bf16 v[12:15], v[144:147], v[172:175], v[12:15]
	v_mfma_f32_16x16x32_bf16 v[8:11], v[136:139], v[168:171], v[8:11]
	v_mfma_f32_16x16x32_bf16 v[4:7], v[144:147], v[168:171], v[4:7]
	v_mfma_f32_16x16x32_bf16 v[32:35], v[140:143], v[196:199], v[32:35]
	v_mfma_f32_16x16x32_bf16 v[28:31], v[148:151], v[196:199], v[28:31]
	v_mfma_f32_16x16x32_bf16 v[24:27], v[140:143], v[192:195], v[24:27]
	v_mfma_f32_16x16x32_bf16 v[20:23], v[148:151], v[192:195], v[20:23]
	v_mfma_f32_16x16x32_bf16 v[16:19], v[140:143], v[188:191], v[16:19]
	v_mfma_f32_16x16x32_bf16 v[12:15], v[148:151], v[188:191], v[12:15]
	v_mfma_f32_16x16x32_bf16 v[8:11], v[140:143], v[184:187], v[8:11]
	v_mfma_f32_16x16x32_bf16 v[4:7], v[148:151], v[184:187], v[4:7]
	s_branch .LBB0_1424
